# SwiGLU epilogue stores of P6/P14 marked nt (streaming outputs should not displace GEMM operands in L2)
# baseline (speedup 1.0000x reference)
; __device__ __forceinline__ unsigned cvt4_fp8(float a, float b, float c, float d) { int w = 0; w = __builtin_amdgcn_cvt_pk_fp8_f32(clamp448(a), clamp448(b), w, false); w = __builtin_amdgcn_cvt_pk_fp8_f32(clamp448(c), clamp448(d), w, true); return (unsigned)w; }
; __device__ __forceinline__ float siluf_(float x) { return x * sigmoidf_(x); }
; __device__ __forceinline__ u32x4 pack8(const f32x4 a, const f32x4 b) { u32x4 w; w.x = cvt_pk_bf16(a[0], a[1]); w.y = cvt_pk_bf16(a[2], a[3]); w.z = cvt_pk_bf16(b[0], b[1]); w.w = cvt_pk_bf16(b[2], b[3]); return w; }
;     __device__ __forceinline__ void operator()(const AccT& acc, const Unit& u, int wr, int wc, int fr, int fq) const {
;         const int row0 = u.orow0 + wr * 64 + fr, cb = u.pn * 128 + wc * 32 + 8 * fq, nb = u.pn * 256 + wc * 32 + 8 * fq;
;         f32x4 cg0 = *(const f32x4*)(cmax + nb) * (1.0f / 127.0f), cg1 = *(const f32x4*)(cmax + nb + 4) * (1.0f / 127.0f), cu0 = *(const f32x4*)(cmax + nb + 128) * (1.0f / 127.0f), cu1 = *(const f32x4*)(cmax + nb + 132) * (1.0f / 127.0f);
; #pragma unroll
;         for (int ai = 0; ai < 2; ++ai)
; #pragma unroll
;             for (int m = 0; m < 4; ++m) { const int row = row0 + ai * HALF + m * 16; const float rs = rsc[row]; f32x4 z0, z1;
;                 const i32x4v g0 = __builtin_bit_cast(i32x4v, acc[ai][0][m][0]), g1 = __builtin_bit_cast(i32x4v, acc[ai][0][m][1]), u0 = __builtin_bit_cast(i32x4v, acc[ai][1][m][0]), u1 = __builtin_bit_cast(i32x4v, acc[ai][1][m][1]);
; #pragma unroll
;                 for (int j = 0; j < 4; ++j) { z0[j] = siluf_((float)g0[j] * (rs * cg0[j])) * ((float)u0[j] * (rs * cu0[j])); z1[j] = siluf_((float)g1[j] * (rs * cg1[j])) * ((float)u1[j] * (rs * cu1[j])); }
;                 if (sout8 > 0.f) { u32x2 w; w.x = cvt4_fp8(z0[0] * sout8, z0[1] * sout8, z0[2] * sout8, z0[3] * sout8); w.y = cvt4_fp8(z1[0] * sout8, z1[1] * sout8, z1[2] * sout8, z1[3] * sout8); *(u32x2*)((unsigned char*)O + (size_t)row * ldo + cb) = w; }
;                 else *(u32x4*)(O + (size_t)row * ldo + cb) = pack8(z0, z1);
;                 __builtin_amdgcn_sched_barrier(0); }
.LBB0_1420:
	v_lshl_or_b32 v130, s63, 8, v177
	v_ashrrev_i32_e32 v131, 31, v130
	v_lshl_add_u64 v[130:131], v[130:131], 2, s[16:17]
	v_add_u32_e32 v132, s62, v175
	global_load_dwordx4 v[136:139], v[130:131], off offset:512
	global_load_dwordx4 v[140:143], v[130:131], off
	global_load_dwordx4 v[144:147], v[130:131], off offset:528
	global_load_dwordx4 v[148:151], v[130:131], off offset:16
	v_ashrrev_i32_e32 v133, 31, v132
	v_lshl_add_u64 v[134:135], v[132:133], 2, s[14:15]
	global_load_dword v152, v[134:135], off
	global_load_dword v211, v[134:135], off offset:64
	global_load_dword v212, v[134:135], off offset:128
	global_load_dword v213, v[134:135], off offset:192
	global_load_dword v214, v[134:135], off offset:512
	global_load_dword v215, v[134:135], off offset:576
	global_load_dword v216, v[134:135], off offset:640
	global_load_dword v217, v[134:135], off offset:704
	s_nop 0
	s_nop 0
	s_nop 0
	s_nop 0
	s_nop 0
	s_nop 0
	s_nop 0
	s_nop 0
	s_nop 0
	s_nop 0
	s_nop 0
	s_nop 0
	s_nop 0
	s_nop 0
	s_nop 0
	s_nop 0
	v_lshl_or_b32 v130, s63, 7, v177
	v_ashrrev_i32_e32 v131, 31, v130
	s_waitcnt vmcnt(0)
	s_mov_b32 s98, 0xbc3a1e78
	s_mov_b32 s100, 0x39820610
	v_pk_mul_f32 v[132:133], v[140:141], s[98:99] op_sel_hi:[1,0]
	v_pk_mul_f32 v[134:135], v[142:143], s[98:99] op_sel_hi:[1,0]
	v_pk_mul_f32 v[154:155], v[148:149], s[98:99] op_sel_hi:[1,0]
	v_pk_mul_f32 v[156:157], v[150:151], s[98:99] op_sel_hi:[1,0]
	v_pk_mul_f32 v[158:159], v[140:141], v[136:137]
	v_pk_mul_f32 v[160:161], v[142:143], v[138:139]
	v_pk_mul_f32 v[186:187], v[148:149], v[144:145]
	v_pk_mul_f32 v[188:189], v[150:151], v[146:147]
	v_add_u32_e32 v207, s62, v175
	v_mov_b64_e32 v[200:201], s[6:7]
	v_pk_mul_f32 v[158:159], v[158:159], s[100:101] op_sel_hi:[1,0]
	v_pk_mul_f32 v[160:161], v[160:161], s[100:101] op_sel_hi:[1,0]
	v_pk_mul_f32 v[186:187], v[186:187], s[100:101] op_sel_hi:[1,0]
	v_pk_mul_f32 v[188:189], v[188:189], s[100:101] op_sel_hi:[1,0]
	v_mad_i64_i32 v[198:199], s[34:35], v207, s59, v[200:201]
	v_lshl_add_u64 v[198:199], v[198:199], 0, v[130:131]
	s_mov_b32 s101, 0
	v_cvt_f32_i32_e32 v126, v126
	v_cvt_f32_i32_e32 v127, v127
	v_cvt_f32_i32_e32 v128, v128
	v_cvt_f32_i32_e32 v129, v129
	v_cvt_f32_i32_e32 v122, v122
	v_cvt_f32_i32_e32 v123, v123
	v_cvt_f32_i32_e32 v124, v124
	v_cvt_f32_i32_e32 v125, v125
	v_cvt_f32_i32_e32 v118, v118
	v_cvt_f32_i32_e32 v119, v119
	v_cvt_f32_i32_e32 v120, v120
	v_cvt_f32_i32_e32 v121, v121
	v_cvt_f32_i32_e32 v114, v114
	v_cvt_f32_i32_e32 v115, v115
	v_cvt_f32_i32_e32 v116, v116
	v_cvt_f32_i32_e32 v117, v117
	v_mul_f32_e32 v206, v152, v152
	v_pk_mul_f32 v[136:137], v[152:153], v[132:133] op_sel_hi:[0,1]
	v_pk_mul_f32 v[138:139], v[152:153], v[134:135] op_sel_hi:[0,1]
	v_pk_mul_f32 v[140:141], v[152:153], v[154:155] op_sel_hi:[0,1]
	v_pk_mul_f32 v[142:143], v[152:153], v[156:157] op_sel_hi:[0,1]
	v_pk_mul_f32 v[190:191], v[126:127], v[136:137]
	v_pk_mul_f32 v[192:193], v[128:129], v[138:139]
	v_pk_mul_f32 v[194:195], v[122:123], v[140:141]
	v_pk_mul_f32 v[196:197], v[124:125], v[142:143]
	v_exp_f32_e32 v190, v190
	v_exp_f32_e32 v191, v191
	v_exp_f32_e32 v192, v192
	v_exp_f32_e32 v193, v193
	v_exp_f32_e32 v194, v194
	v_exp_f32_e32 v195, v195
	v_exp_f32_e32 v196, v196
	v_exp_f32_e32 v197, v197
	v_pk_mul_f32 v[118:119], v[126:127], v[118:119]
	v_pk_mul_f32 v[120:121], v[128:129], v[120:121]
	v_pk_mul_f32 v[114:115], v[122:123], v[114:115]
	v_pk_mul_f32 v[116:117], v[124:125], v[116:117]
	v_pk_mul_f32 v[144:145], v[206:207], v[158:159] op_sel_hi:[0,1]
	v_pk_mul_f32 v[146:147], v[206:207], v[160:161] op_sel_hi:[0,1]
	v_pk_mul_f32 v[148:149], v[206:207], v[186:187] op_sel_hi:[0,1]
	v_pk_mul_f32 v[150:151], v[206:207], v[188:189] op_sel_hi:[0,1]
	v_pk_add_f32 v[190:191], v[190:191], 1.0 op_sel_hi:[1,0]
	v_pk_add_f32 v[192:193], v[192:193], 1.0 op_sel_hi:[1,0]
	v_pk_add_f32 v[194:195], v[194:195], 1.0 op_sel_hi:[1,0]
	v_pk_add_f32 v[196:197], v[196:197], 1.0 op_sel_hi:[1,0]
	v_rcp_f32_e32 v190, v190
	v_rcp_f32_e32 v191, v191
	v_rcp_f32_e32 v192, v192
	v_rcp_f32_e32 v193, v193
	v_rcp_f32_e32 v194, v194
	v_rcp_f32_e32 v195, v195
	v_rcp_f32_e32 v196, v196
	v_rcp_f32_e32 v197, v197
	v_pk_mul_f32 v[118:119], v[118:119], v[144:145]
	v_pk_mul_f32 v[120:121], v[120:121], v[146:147]
	v_pk_mul_f32 v[114:115], v[114:115], v[148:149]
	v_pk_mul_f32 v[116:117], v[116:117], v[150:151]
	s_mov_b32 s100, 0x0
	v_pk_mul_f32 v[118:119], v[118:119], v[190:191]
	v_pk_mul_f32 v[120:121], v[120:121], v[192:193]
	v_pk_mul_f32 v[114:115], v[114:115], v[194:195]
	v_pk_mul_f32 v[116:117], v[116:117], v[196:197]
	v_med3_f32 v118, v118, s58, v181
	v_med3_f32 v119, v119, s58, v181
	v_med3_f32 v120, v120, s58, v181
	v_med3_f32 v121, v121, s58, v181
	v_med3_f32 v114, v114, s58, v181
	v_med3_f32 v115, v115, s58, v181
	v_med3_f32 v116, v116, s58, v181
	v_med3_f32 v117, v117, s58, v181
	v_cvt_pk_fp8_f32 v204, v118, v119
	v_cvt_pk_fp8_f32 v205, v114, v115
	v_lshl_add_u64 v[202:203], v[198:199], 0, s[100:101]
	v_cvt_pk_fp8_f32 v204, v120, v121 op_sel:[0,0,1]
	v_cvt_pk_fp8_f32 v205, v116, v117 op_sel:[0,0,1]
	s_nop 0
	global_store_dwordx2 v[202:203], v[204:205], off nt
	v_cvt_f32_i32_e32 v110, v110
	v_cvt_f32_i32_e32 v111, v111
	v_cvt_f32_i32_e32 v112, v112
	v_cvt_f32_i32_e32 v113, v113
	v_cvt_f32_i32_e32 v106, v106
	v_cvt_f32_i32_e32 v107, v107
	v_cvt_f32_i32_e32 v108, v108
	v_cvt_f32_i32_e32 v109, v109
	v_cvt_f32_i32_e32 v102, v102
	v_cvt_f32_i32_e32 v103, v103
	v_cvt_f32_i32_e32 v104, v104
	v_cvt_f32_i32_e32 v105, v105
	v_cvt_f32_i32_e32 v98, v98
	v_cvt_f32_i32_e32 v99, v99
	v_cvt_f32_i32_e32 v100, v100
	v_cvt_f32_i32_e32 v101, v101
	v_mul_f32_e32 v206, v211, v211
; __device__ __forceinline__ unsigned cvt4_fp8(float a, float b, float c, float d) { int w = 0; w = __builtin_amdgcn_cvt_pk_fp8_f32(clamp448(a), clamp448(b), w, false); w = __builtin_amdgcn_cvt_pk_fp8_f32(clamp448(c), clamp448(d), w, true); return (unsigned)w; }
; __device__ __forceinline__ float siluf_(float x) { return x * sigmoidf_(x); }
; __device__ __forceinline__ u32x4 pack8(const f32x4 a, const f32x4 b) { u32x4 w; w.x = cvt_pk_bf16(a[0], a[1]); w.y = cvt_pk_bf16(a[2], a[3]); w.z = cvt_pk_bf16(b[0], b[1]); w.w = cvt_pk_bf16(b[2], b[3]); return w; }
;     __device__ __forceinline__ void operator()(const AccT& acc, const Unit& u, int wr, int wc, int fr, int fq) const {
;     ...
;             for (int m = 0; m < 4; ++m) { const int row = row0 + ai * HALF + m * 16; const float rs = rsc[row]; f32x4 z0, z1;
;                 const i32x4v g0 = __builtin_bit_cast(i32x4v, acc[ai][0][m][0]), g1 = __builtin_bit_cast(i32x4v, acc[ai][0][m][1]), u0 = __builtin_bit_cast(i32x4v, acc[ai][1][m][0]), u1 = __builtin_bit_cast(i32x4v, acc[ai][1][m][1]);
; #pragma unroll
;                 for (int j = 0; j < 4; ++j) { z0[j] = siluf_((float)g0[j] * (rs * cg0[j])) * ((float)u0[j] * (rs * cu0[j])); z1[j] = siluf_((float)g1[j] * (rs * cg1[j])) * ((float)u1[j] * (rs * cu1[j])); }
;                 if (sout8 > 0.f) { u32x2 w; w.x = cvt4_fp8(z0[0] * sout8, z0[1] * sout8, z0[2] * sout8, z0[3] * sout8); w.y = cvt4_fp8(z1[0] * sout8, z1[1] * sout8, z1[2] * sout8, z1[3] * sout8); *(u32x2*)((unsigned char*)O + (size_t)row * ldo + cb) = w; }
;                 else *(u32x4*)(O + (size_t)row * ldo + cb) = pack8(z0, z1);
;                 __builtin_amdgcn_sched_barrier(0); }
	v_pk_mul_f32 v[136:137], v[210:211], v[132:133] op_sel:[1,0] op_sel_hi:[1,1]
	v_pk_mul_f32 v[138:139], v[210:211], v[134:135] op_sel:[1,0] op_sel_hi:[1,1]
	v_pk_mul_f32 v[140:141], v[210:211], v[154:155] op_sel:[1,0] op_sel_hi:[1,1]
	v_pk_mul_f32 v[142:143], v[210:211], v[156:157] op_sel:[1,0] op_sel_hi:[1,1]
	v_pk_mul_f32 v[190:191], v[110:111], v[136:137]
	v_pk_mul_f32 v[192:193], v[112:113], v[138:139]
	v_pk_mul_f32 v[194:195], v[106:107], v[140:141]
	v_pk_mul_f32 v[196:197], v[108:109], v[142:143]
	v_exp_f32_e32 v190, v190
	v_exp_f32_e32 v191, v191
	v_exp_f32_e32 v192, v192
	v_exp_f32_e32 v193, v193
	v_exp_f32_e32 v194, v194
	v_exp_f32_e32 v195, v195
	v_exp_f32_e32 v196, v196
	v_exp_f32_e32 v197, v197
	v_pk_mul_f32 v[102:103], v[110:111], v[102:103]
	v_pk_mul_f32 v[104:105], v[112:113], v[104:105]
	v_pk_mul_f32 v[98:99], v[106:107], v[98:99]
	v_pk_mul_f32 v[100:101], v[108:109], v[100:101]
	v_pk_mul_f32 v[144:145], v[206:207], v[158:159] op_sel_hi:[0,1]
	v_pk_mul_f32 v[146:147], v[206:207], v[160:161] op_sel_hi:[0,1]
	v_pk_mul_f32 v[148:149], v[206:207], v[186:187] op_sel_hi:[0,1]
	v_pk_mul_f32 v[150:151], v[206:207], v[188:189] op_sel_hi:[0,1]
	v_pk_add_f32 v[190:191], v[190:191], 1.0 op_sel_hi:[1,0]
	v_pk_add_f32 v[192:193], v[192:193], 1.0 op_sel_hi:[1,0]
	v_pk_add_f32 v[194:195], v[194:195], 1.0 op_sel_hi:[1,0]
	v_pk_add_f32 v[196:197], v[196:197], 1.0 op_sel_hi:[1,0]
	v_rcp_f32_e32 v190, v190
	v_rcp_f32_e32 v191, v191
	v_rcp_f32_e32 v192, v192
	v_rcp_f32_e32 v193, v193
	v_rcp_f32_e32 v194, v194
	v_rcp_f32_e32 v195, v195
	v_rcp_f32_e32 v196, v196
	v_rcp_f32_e32 v197, v197
	v_pk_mul_f32 v[102:103], v[102:103], v[144:145]
	v_pk_mul_f32 v[104:105], v[104:105], v[146:147]
	v_pk_mul_f32 v[98:99], v[98:99], v[148:149]
	v_pk_mul_f32 v[100:101], v[100:101], v[150:151]
	s_mov_b32 s100, 0x16000
	v_pk_mul_f32 v[102:103], v[102:103], v[190:191]
	v_pk_mul_f32 v[104:105], v[104:105], v[192:193]
	v_pk_mul_f32 v[98:99], v[98:99], v[194:195]
	v_pk_mul_f32 v[100:101], v[100:101], v[196:197]
	v_med3_f32 v102, v102, s58, v181
	v_med3_f32 v103, v103, s58, v181
	v_med3_f32 v104, v104, s58, v181
	v_med3_f32 v105, v105, s58, v181
	v_med3_f32 v98, v98, s58, v181
	v_med3_f32 v99, v99, s58, v181
	v_med3_f32 v100, v100, s58, v181
	v_med3_f32 v101, v101, s58, v181
	v_cvt_pk_fp8_f32 v204, v102, v103
	v_cvt_pk_fp8_f32 v205, v98, v99
	v_lshl_add_u64 v[202:203], v[198:199], 0, s[100:101]
	v_cvt_pk_fp8_f32 v204, v104, v105 op_sel:[0,0,1]
	v_cvt_pk_fp8_f32 v205, v100, v101 op_sel:[0,0,1]
	s_nop 0
	global_store_dwordx2 v[202:203], v[204:205], off nt
	v_cvt_f32_i32_e32 v94, v94
	v_cvt_f32_i32_e32 v95, v95
	v_cvt_f32_i32_e32 v96, v96
	v_cvt_f32_i32_e32 v97, v97
	v_cvt_f32_i32_e32 v90, v90
	v_cvt_f32_i32_e32 v91, v91
	v_cvt_f32_i32_e32 v92, v92
	v_cvt_f32_i32_e32 v93, v93
	v_cvt_f32_i32_e32 v86, v86
	v_cvt_f32_i32_e32 v87, v87
	v_cvt_f32_i32_e32 v88, v88
	v_cvt_f32_i32_e32 v89, v89
	v_cvt_f32_i32_e32 v82, v82
	v_cvt_f32_i32_e32 v83, v83
	v_cvt_f32_i32_e32 v84, v84
	v_cvt_f32_i32_e32 v85, v85
	v_mul_f32_e32 v206, v212, v212
	v_pk_mul_f32 v[136:137], v[212:213], v[132:133] op_sel_hi:[0,1]
	v_pk_mul_f32 v[138:139], v[212:213], v[134:135] op_sel_hi:[0,1]
	v_pk_mul_f32 v[140:141], v[212:213], v[154:155] op_sel_hi:[0,1]
	v_pk_mul_f32 v[142:143], v[212:213], v[156:157] op_sel_hi:[0,1]
	v_pk_mul_f32 v[190:191], v[94:95], v[136:137]
	v_pk_mul_f32 v[192:193], v[96:97], v[138:139]
	v_pk_mul_f32 v[194:195], v[90:91], v[140:141]
	v_pk_mul_f32 v[196:197], v[92:93], v[142:143]
	v_exp_f32_e32 v190, v190
	v_exp_f32_e32 v191, v191
	v_exp_f32_e32 v192, v192
	v_exp_f32_e32 v193, v193
	v_exp_f32_e32 v194, v194
	v_exp_f32_e32 v195, v195
	v_exp_f32_e32 v196, v196
	v_exp_f32_e32 v197, v197
	v_pk_mul_f32 v[86:87], v[94:95], v[86:87]
	v_pk_mul_f32 v[88:89], v[96:97], v[88:89]
	v_pk_mul_f32 v[82:83], v[90:91], v[82:83]
	v_pk_mul_f32 v[84:85], v[92:93], v[84:85]
	v_pk_mul_f32 v[144:145], v[206:207], v[158:159] op_sel_hi:[0,1]
	v_pk_mul_f32 v[146:147], v[206:207], v[160:161] op_sel_hi:[0,1]
	v_pk_mul_f32 v[148:149], v[206:207], v[186:187] op_sel_hi:[0,1]
	v_pk_mul_f32 v[150:151], v[206:207], v[188:189] op_sel_hi:[0,1]
	v_pk_add_f32 v[190:191], v[190:191], 1.0 op_sel_hi:[1,0]
	v_pk_add_f32 v[192:193], v[192:193], 1.0 op_sel_hi:[1,0]
	v_pk_add_f32 v[194:195], v[194:195], 1.0 op_sel_hi:[1,0]
	v_pk_add_f32 v[196:197], v[196:197], 1.0 op_sel_hi:[1,0]
	v_rcp_f32_e32 v190, v190
	v_rcp_f32_e32 v191, v191
	v_rcp_f32_e32 v192, v192
	v_rcp_f32_e32 v193, v193
	v_rcp_f32_e32 v194, v194
	v_rcp_f32_e32 v195, v195
	v_rcp_f32_e32 v196, v196
	v_rcp_f32_e32 v197, v197
	v_pk_mul_f32 v[86:87], v[86:87], v[144:145]
	v_pk_mul_f32 v[88:89], v[88:89], v[146:147]
	v_pk_mul_f32 v[82:83], v[82:83], v[148:149]
	v_pk_mul_f32 v[84:85], v[84:85], v[150:151]
	s_mov_b32 s100, 0x2c000
	v_pk_mul_f32 v[86:87], v[86:87], v[190:191]
	v_pk_mul_f32 v[88:89], v[88:89], v[192:193]
	v_pk_mul_f32 v[82:83], v[82:83], v[194:195]
	v_pk_mul_f32 v[84:85], v[84:85], v[196:197]
	v_med3_f32 v86, v86, s58, v181
	v_med3_f32 v87, v87, s58, v181
	v_med3_f32 v88, v88, s58, v181
	v_med3_f32 v89, v89, s58, v181
	v_med3_f32 v82, v82, s58, v181
	v_med3_f32 v83, v83, s58, v181
	v_med3_f32 v84, v84, s58, v181
	v_med3_f32 v85, v85, s58, v181
	v_cvt_pk_fp8_f32 v204, v86, v87
	v_cvt_pk_fp8_f32 v205, v82, v83
	v_lshl_add_u64 v[202:203], v[198:199], 0, s[100:101]
	v_cvt_pk_fp8_f32 v204, v88, v89 op_sel:[0,0,1]
	v_cvt_pk_fp8_f32 v205, v84, v85 op_sel:[0,0,1]
	s_nop 0
	global_store_dwordx2 v[202:203], v[204:205], off nt
	v_cvt_f32_i32_e32 v78, v78
	v_cvt_f32_i32_e32 v79, v79
	v_cvt_f32_i32_e32 v80, v80
	v_cvt_f32_i32_e32 v81, v81
	v_cvt_f32_i32_e32 v74, v74
; __device__ __forceinline__ unsigned cvt4_fp8(float a, float b, float c, float d) { int w = 0; w = __builtin_amdgcn_cvt_pk_fp8_f32(clamp448(a), clamp448(b), w, false); w = __builtin_amdgcn_cvt_pk_fp8_f32(clamp448(c), clamp448(d), w, true); return (unsigned)w; }
; __device__ __forceinline__ float siluf_(float x) { return x * sigmoidf_(x); }
; __device__ __forceinline__ u32x4 pack8(const f32x4 a, const f32x4 b) { u32x4 w; w.x = cvt_pk_bf16(a[0], a[1]); w.y = cvt_pk_bf16(a[2], a[3]); w.z = cvt_pk_bf16(b[0], b[1]); w.w = cvt_pk_bf16(b[2], b[3]); return w; }
;     __device__ __forceinline__ void operator()(const AccT& acc, const Unit& u, int wr, int wc, int fr, int fq) const {
;     ...
;             for (int m = 0; m < 4; ++m) { const int row = row0 + ai * HALF + m * 16; const float rs = rsc[row]; f32x4 z0, z1;
;                 const i32x4v g0 = __builtin_bit_cast(i32x4v, acc[ai][0][m][0]), g1 = __builtin_bit_cast(i32x4v, acc[ai][0][m][1]), u0 = __builtin_bit_cast(i32x4v, acc[ai][1][m][0]), u1 = __builtin_bit_cast(i32x4v, acc[ai][1][m][1]);
; #pragma unroll
;                 for (int j = 0; j < 4; ++j) { z0[j] = siluf_((float)g0[j] * (rs * cg0[j])) * ((float)u0[j] * (rs * cu0[j])); z1[j] = siluf_((float)g1[j] * (rs * cg1[j])) * ((float)u1[j] * (rs * cu1[j])); }
;                 if (sout8 > 0.f) { u32x2 w; w.x = cvt4_fp8(z0[0] * sout8, z0[1] * sout8, z0[2] * sout8, z0[3] * sout8); w.y = cvt4_fp8(z1[0] * sout8, z1[1] * sout8, z1[2] * sout8, z1[3] * sout8); *(u32x2*)((unsigned char*)O + (size_t)row * ldo + cb) = w; }
;                 else *(u32x4*)(O + (size_t)row * ldo + cb) = pack8(z0, z1);
;                 __builtin_amdgcn_sched_barrier(0); }
	v_cvt_f32_i32_e32 v75, v75
	v_cvt_f32_i32_e32 v76, v76
	v_cvt_f32_i32_e32 v77, v77
	v_cvt_f32_i32_e32 v70, v70
	v_cvt_f32_i32_e32 v71, v71
	v_cvt_f32_i32_e32 v72, v72
	v_cvt_f32_i32_e32 v73, v73
	v_cvt_f32_i32_e32 v66, v66
	v_cvt_f32_i32_e32 v67, v67
	v_cvt_f32_i32_e32 v68, v68
	v_cvt_f32_i32_e32 v69, v69
	v_mul_f32_e32 v206, v213, v213
	v_pk_mul_f32 v[136:137], v[212:213], v[132:133] op_sel:[1,0] op_sel_hi:[1,1]
	v_pk_mul_f32 v[138:139], v[212:213], v[134:135] op_sel:[1,0] op_sel_hi:[1,1]
	v_pk_mul_f32 v[140:141], v[212:213], v[154:155] op_sel:[1,0] op_sel_hi:[1,1]
	v_pk_mul_f32 v[142:143], v[212:213], v[156:157] op_sel:[1,0] op_sel_hi:[1,1]
	v_pk_mul_f32 v[190:191], v[78:79], v[136:137]
	v_pk_mul_f32 v[192:193], v[80:81], v[138:139]
	v_pk_mul_f32 v[194:195], v[74:75], v[140:141]
	v_pk_mul_f32 v[196:197], v[76:77], v[142:143]
	v_exp_f32_e32 v190, v190
	v_exp_f32_e32 v191, v191
	v_exp_f32_e32 v192, v192
	v_exp_f32_e32 v193, v193
	v_exp_f32_e32 v194, v194
	v_exp_f32_e32 v195, v195
	v_exp_f32_e32 v196, v196
	v_exp_f32_e32 v197, v197
	v_pk_mul_f32 v[70:71], v[78:79], v[70:71]
	v_pk_mul_f32 v[72:73], v[80:81], v[72:73]
	v_pk_mul_f32 v[66:67], v[74:75], v[66:67]
	v_pk_mul_f32 v[68:69], v[76:77], v[68:69]
	v_pk_mul_f32 v[144:145], v[206:207], v[158:159] op_sel_hi:[0,1]
	v_pk_mul_f32 v[146:147], v[206:207], v[160:161] op_sel_hi:[0,1]
	v_pk_mul_f32 v[148:149], v[206:207], v[186:187] op_sel_hi:[0,1]
	v_pk_mul_f32 v[150:151], v[206:207], v[188:189] op_sel_hi:[0,1]
	v_pk_add_f32 v[190:191], v[190:191], 1.0 op_sel_hi:[1,0]
	v_pk_add_f32 v[192:193], v[192:193], 1.0 op_sel_hi:[1,0]
	v_pk_add_f32 v[194:195], v[194:195], 1.0 op_sel_hi:[1,0]
	v_pk_add_f32 v[196:197], v[196:197], 1.0 op_sel_hi:[1,0]
	v_rcp_f32_e32 v190, v190
	v_rcp_f32_e32 v191, v191
	v_rcp_f32_e32 v192, v192
	v_rcp_f32_e32 v193, v193
	v_rcp_f32_e32 v194, v194
	v_rcp_f32_e32 v195, v195
	v_rcp_f32_e32 v196, v196
	v_rcp_f32_e32 v197, v197
	v_pk_mul_f32 v[70:71], v[70:71], v[144:145]
	v_pk_mul_f32 v[72:73], v[72:73], v[146:147]
	v_pk_mul_f32 v[66:67], v[66:67], v[148:149]
	v_pk_mul_f32 v[68:69], v[68:69], v[150:151]
	s_mov_b32 s100, 0x42000
	v_pk_mul_f32 v[70:71], v[70:71], v[190:191]
	v_pk_mul_f32 v[72:73], v[72:73], v[192:193]
	v_pk_mul_f32 v[66:67], v[66:67], v[194:195]
	v_pk_mul_f32 v[68:69], v[68:69], v[196:197]
	v_med3_f32 v70, v70, s58, v181
	v_med3_f32 v71, v71, s58, v181
	v_med3_f32 v72, v72, s58, v181
	v_med3_f32 v73, v73, s58, v181
	v_med3_f32 v66, v66, s58, v181
	v_med3_f32 v67, v67, s58, v181
	v_med3_f32 v68, v68, s58, v181
	v_med3_f32 v69, v69, s58, v181
	v_cvt_pk_fp8_f32 v204, v70, v71
	v_cvt_pk_fp8_f32 v205, v66, v67
	v_lshl_add_u64 v[202:203], v[198:199], 0, s[100:101]
	v_cvt_pk_fp8_f32 v204, v72, v73 op_sel:[0,0,1]
	v_cvt_pk_fp8_f32 v205, v68, v69 op_sel:[0,0,1]
	s_nop 0
	global_store_dwordx2 v[202:203], v[204:205], off nt
	v_cvt_f32_i32_e32 v62, v62
	v_cvt_f32_i32_e32 v63, v63
	v_cvt_f32_i32_e32 v64, v64
	v_cvt_f32_i32_e32 v65, v65
	v_cvt_f32_i32_e32 v58, v58
	v_cvt_f32_i32_e32 v59, v59
	v_cvt_f32_i32_e32 v60, v60
	v_cvt_f32_i32_e32 v61, v61
	v_cvt_f32_i32_e32 v54, v54
	v_cvt_f32_i32_e32 v55, v55
	v_cvt_f32_i32_e32 v56, v56
	v_cvt_f32_i32_e32 v57, v57
	v_cvt_f32_i32_e32 v50, v50
	v_cvt_f32_i32_e32 v51, v51
	v_cvt_f32_i32_e32 v52, v52
	v_cvt_f32_i32_e32 v53, v53
	v_mul_f32_e32 v206, v214, v214
	v_pk_mul_f32 v[136:137], v[214:215], v[132:133] op_sel_hi:[0,1]
	v_pk_mul_f32 v[138:139], v[214:215], v[134:135] op_sel_hi:[0,1]
	v_pk_mul_f32 v[140:141], v[214:215], v[154:155] op_sel_hi:[0,1]
	v_pk_mul_f32 v[142:143], v[214:215], v[156:157] op_sel_hi:[0,1]
	v_pk_mul_f32 v[190:191], v[62:63], v[136:137]
	v_pk_mul_f32 v[192:193], v[64:65], v[138:139]
	v_pk_mul_f32 v[194:195], v[58:59], v[140:141]
	v_pk_mul_f32 v[196:197], v[60:61], v[142:143]
	v_exp_f32_e32 v190, v190
	v_exp_f32_e32 v191, v191
	v_exp_f32_e32 v192, v192
	v_exp_f32_e32 v193, v193
	v_exp_f32_e32 v194, v194
	v_exp_f32_e32 v195, v195
	v_exp_f32_e32 v196, v196
	v_exp_f32_e32 v197, v197
	v_pk_mul_f32 v[54:55], v[62:63], v[54:55]
	v_pk_mul_f32 v[56:57], v[64:65], v[56:57]
	v_pk_mul_f32 v[50:51], v[58:59], v[50:51]
	v_pk_mul_f32 v[52:53], v[60:61], v[52:53]
	v_pk_mul_f32 v[144:145], v[206:207], v[158:159] op_sel_hi:[0,1]
	v_pk_mul_f32 v[146:147], v[206:207], v[160:161] op_sel_hi:[0,1]
	v_pk_mul_f32 v[148:149], v[206:207], v[186:187] op_sel_hi:[0,1]
	v_pk_mul_f32 v[150:151], v[206:207], v[188:189] op_sel_hi:[0,1]
	v_pk_add_f32 v[190:191], v[190:191], 1.0 op_sel_hi:[1,0]
	v_pk_add_f32 v[192:193], v[192:193], 1.0 op_sel_hi:[1,0]
	v_pk_add_f32 v[194:195], v[194:195], 1.0 op_sel_hi:[1,0]
	v_pk_add_f32 v[196:197], v[196:197], 1.0 op_sel_hi:[1,0]
	v_rcp_f32_e32 v190, v190
	v_rcp_f32_e32 v191, v191
	v_rcp_f32_e32 v192, v192
	v_rcp_f32_e32 v193, v193
	v_rcp_f32_e32 v194, v194
	v_rcp_f32_e32 v195, v195
	v_rcp_f32_e32 v196, v196
	v_rcp_f32_e32 v197, v197
	v_pk_mul_f32 v[54:55], v[54:55], v[144:145]
	v_pk_mul_f32 v[56:57], v[56:57], v[146:147]
	v_pk_mul_f32 v[50:51], v[50:51], v[148:149]
	v_pk_mul_f32 v[52:53], v[52:53], v[150:151]
	s_mov_b32 s100, 0xb0000
	v_pk_mul_f32 v[54:55], v[54:55], v[190:191]
	v_pk_mul_f32 v[56:57], v[56:57], v[192:193]
	v_pk_mul_f32 v[50:51], v[50:51], v[194:195]
	v_pk_mul_f32 v[52:53], v[52:53], v[196:197]
	v_med3_f32 v54, v54, s58, v181
	v_med3_f32 v55, v55, s58, v181
	v_med3_f32 v56, v56, s58, v181
	v_med3_f32 v57, v57, s58, v181
	v_med3_f32 v50, v50, s58, v181
	v_med3_f32 v51, v51, s58, v181
	v_med3_f32 v52, v52, s58, v181
	v_med3_f32 v53, v53, s58, v181
	v_cvt_pk_fp8_f32 v204, v54, v55
	v_cvt_pk_fp8_f32 v205, v50, v51
	v_lshl_add_u64 v[202:203], v[198:199], 0, s[100:101]
	v_cvt_pk_fp8_f32 v204, v56, v57 op_sel:[0,0,1]
; __device__ __forceinline__ unsigned cvt4_fp8(float a, float b, float c, float d) { int w = 0; w = __builtin_amdgcn_cvt_pk_fp8_f32(clamp448(a), clamp448(b), w, false); w = __builtin_amdgcn_cvt_pk_fp8_f32(clamp448(c), clamp448(d), w, true); return (unsigned)w; }
; __device__ __forceinline__ float siluf_(float x) { return x * sigmoidf_(x); }
; __device__ __forceinline__ u32x4 pack8(const f32x4 a, const f32x4 b) { u32x4 w; w.x = cvt_pk_bf16(a[0], a[1]); w.y = cvt_pk_bf16(a[2], a[3]); w.z = cvt_pk_bf16(b[0], b[1]); w.w = cvt_pk_bf16(b[2], b[3]); return w; }
;     __device__ __forceinline__ void operator()(const AccT& acc, const Unit& u, int wr, int wc, int fr, int fq) const {
;     ...
;             for (int m = 0; m < 4; ++m) { const int row = row0 + ai * HALF + m * 16; const float rs = rsc[row]; f32x4 z0, z1;
;                 const i32x4v g0 = __builtin_bit_cast(i32x4v, acc[ai][0][m][0]), g1 = __builtin_bit_cast(i32x4v, acc[ai][0][m][1]), u0 = __builtin_bit_cast(i32x4v, acc[ai][1][m][0]), u1 = __builtin_bit_cast(i32x4v, acc[ai][1][m][1]);
; #pragma unroll
;                 for (int j = 0; j < 4; ++j) { z0[j] = siluf_((float)g0[j] * (rs * cg0[j])) * ((float)u0[j] * (rs * cu0[j])); z1[j] = siluf_((float)g1[j] * (rs * cg1[j])) * ((float)u1[j] * (rs * cu1[j])); }
;                 if (sout8 > 0.f) { u32x2 w; w.x = cvt4_fp8(z0[0] * sout8, z0[1] * sout8, z0[2] * sout8, z0[3] * sout8); w.y = cvt4_fp8(z1[0] * sout8, z1[1] * sout8, z1[2] * sout8, z1[3] * sout8); *(u32x2*)((unsigned char*)O + (size_t)row * ldo + cb) = w; }
;                 else *(u32x4*)(O + (size_t)row * ldo + cb) = pack8(z0, z1);
;                 __builtin_amdgcn_sched_barrier(0); }
	v_cvt_pk_fp8_f32 v205, v52, v53 op_sel:[0,0,1]
	s_nop 0
	global_store_dwordx2 v[202:203], v[204:205], off nt
	v_cvt_f32_i32_e32 v46, v46
	v_cvt_f32_i32_e32 v47, v47
	v_cvt_f32_i32_e32 v48, v48
	v_cvt_f32_i32_e32 v49, v49
	v_cvt_f32_i32_e32 v42, v42
	v_cvt_f32_i32_e32 v43, v43
	v_cvt_f32_i32_e32 v44, v44
	v_cvt_f32_i32_e32 v45, v45
	v_cvt_f32_i32_e32 v38, v38
	v_cvt_f32_i32_e32 v39, v39
	v_cvt_f32_i32_e32 v40, v40
	v_cvt_f32_i32_e32 v41, v41
	v_cvt_f32_i32_e32 v34, v34
	v_cvt_f32_i32_e32 v35, v35
	v_cvt_f32_i32_e32 v36, v36
	v_cvt_f32_i32_e32 v37, v37
	v_mul_f32_e32 v206, v215, v215
	v_pk_mul_f32 v[136:137], v[214:215], v[132:133] op_sel:[1,0] op_sel_hi:[1,1]
	v_pk_mul_f32 v[138:139], v[214:215], v[134:135] op_sel:[1,0] op_sel_hi:[1,1]
	v_pk_mul_f32 v[140:141], v[214:215], v[154:155] op_sel:[1,0] op_sel_hi:[1,1]
	v_pk_mul_f32 v[142:143], v[214:215], v[156:157] op_sel:[1,0] op_sel_hi:[1,1]
	v_pk_mul_f32 v[190:191], v[46:47], v[136:137]
	v_pk_mul_f32 v[192:193], v[48:49], v[138:139]
	v_pk_mul_f32 v[194:195], v[42:43], v[140:141]
	v_pk_mul_f32 v[196:197], v[44:45], v[142:143]
	v_exp_f32_e32 v190, v190
	v_exp_f32_e32 v191, v191
	v_exp_f32_e32 v192, v192
	v_exp_f32_e32 v193, v193
	v_exp_f32_e32 v194, v194
	v_exp_f32_e32 v195, v195
	v_exp_f32_e32 v196, v196
	v_exp_f32_e32 v197, v197
	v_pk_mul_f32 v[38:39], v[46:47], v[38:39]
	v_pk_mul_f32 v[40:41], v[48:49], v[40:41]
	v_pk_mul_f32 v[34:35], v[42:43], v[34:35]
	v_pk_mul_f32 v[36:37], v[44:45], v[36:37]
	v_pk_mul_f32 v[144:145], v[206:207], v[158:159] op_sel_hi:[0,1]
	v_pk_mul_f32 v[146:147], v[206:207], v[160:161] op_sel_hi:[0,1]
	v_pk_mul_f32 v[148:149], v[206:207], v[186:187] op_sel_hi:[0,1]
	v_pk_mul_f32 v[150:151], v[206:207], v[188:189] op_sel_hi:[0,1]
	v_pk_add_f32 v[190:191], v[190:191], 1.0 op_sel_hi:[1,0]
	v_pk_add_f32 v[192:193], v[192:193], 1.0 op_sel_hi:[1,0]
	v_pk_add_f32 v[194:195], v[194:195], 1.0 op_sel_hi:[1,0]
	v_pk_add_f32 v[196:197], v[196:197], 1.0 op_sel_hi:[1,0]
	v_rcp_f32_e32 v190, v190
	v_rcp_f32_e32 v191, v191
	v_rcp_f32_e32 v192, v192
	v_rcp_f32_e32 v193, v193
	v_rcp_f32_e32 v194, v194
	v_rcp_f32_e32 v195, v195
	v_rcp_f32_e32 v196, v196
	v_rcp_f32_e32 v197, v197
	v_pk_mul_f32 v[38:39], v[38:39], v[144:145]
	v_pk_mul_f32 v[40:41], v[40:41], v[146:147]
	v_pk_mul_f32 v[34:35], v[34:35], v[148:149]
	v_pk_mul_f32 v[36:37], v[36:37], v[150:151]
	s_mov_b32 s100, 0xc6000
	v_pk_mul_f32 v[38:39], v[38:39], v[190:191]
	v_pk_mul_f32 v[40:41], v[40:41], v[192:193]
	v_pk_mul_f32 v[34:35], v[34:35], v[194:195]
	v_pk_mul_f32 v[36:37], v[36:37], v[196:197]
	v_med3_f32 v38, v38, s58, v181
	v_med3_f32 v39, v39, s58, v181
	v_med3_f32 v40, v40, s58, v181
	v_med3_f32 v41, v41, s58, v181
	v_med3_f32 v34, v34, s58, v181
	v_med3_f32 v35, v35, s58, v181
	v_med3_f32 v36, v36, s58, v181
	v_med3_f32 v37, v37, s58, v181
	v_cvt_pk_fp8_f32 v204, v38, v39
	v_cvt_pk_fp8_f32 v205, v34, v35
	v_lshl_add_u64 v[202:203], v[198:199], 0, s[100:101]
	v_cvt_pk_fp8_f32 v204, v40, v41 op_sel:[0,0,1]
	v_cvt_pk_fp8_f32 v205, v36, v37 op_sel:[0,0,1]
	s_nop 0
	global_store_dwordx2 v[202:203], v[204:205], off nt
	v_cvt_f32_i32_e32 v30, v30
	v_cvt_f32_i32_e32 v31, v31
	v_cvt_f32_i32_e32 v32, v32
	v_cvt_f32_i32_e32 v33, v33
	v_cvt_f32_i32_e32 v26, v26
	v_cvt_f32_i32_e32 v27, v27
	v_cvt_f32_i32_e32 v28, v28
	v_cvt_f32_i32_e32 v29, v29
	v_cvt_f32_i32_e32 v22, v22
	v_cvt_f32_i32_e32 v23, v23
	v_cvt_f32_i32_e32 v24, v24
	v_cvt_f32_i32_e32 v25, v25
	v_cvt_f32_i32_e32 v18, v18
	v_cvt_f32_i32_e32 v19, v19
	v_cvt_f32_i32_e32 v20, v20
	v_cvt_f32_i32_e32 v21, v21
	v_mul_f32_e32 v206, v216, v216
	v_pk_mul_f32 v[136:137], v[216:217], v[132:133] op_sel_hi:[0,1]
	v_pk_mul_f32 v[138:139], v[216:217], v[134:135] op_sel_hi:[0,1]
	v_pk_mul_f32 v[140:141], v[216:217], v[154:155] op_sel_hi:[0,1]
	v_pk_mul_f32 v[142:143], v[216:217], v[156:157] op_sel_hi:[0,1]
	v_pk_mul_f32 v[190:191], v[30:31], v[136:137]
	v_pk_mul_f32 v[192:193], v[32:33], v[138:139]
	v_pk_mul_f32 v[194:195], v[26:27], v[140:141]
	v_pk_mul_f32 v[196:197], v[28:29], v[142:143]
	v_exp_f32_e32 v190, v190
	v_exp_f32_e32 v191, v191
	v_exp_f32_e32 v192, v192
	v_exp_f32_e32 v193, v193
	v_exp_f32_e32 v194, v194
	v_exp_f32_e32 v195, v195
	v_exp_f32_e32 v196, v196
	v_exp_f32_e32 v197, v197
	v_pk_mul_f32 v[22:23], v[30:31], v[22:23]
	v_pk_mul_f32 v[24:25], v[32:33], v[24:25]
	v_pk_mul_f32 v[18:19], v[26:27], v[18:19]
	v_pk_mul_f32 v[20:21], v[28:29], v[20:21]
	v_pk_mul_f32 v[144:145], v[206:207], v[158:159] op_sel_hi:[0,1]
	v_pk_mul_f32 v[146:147], v[206:207], v[160:161] op_sel_hi:[0,1]
; __device__ __forceinline__ unsigned cvt4_fp8(float a, float b, float c, float d) { int w = 0; w = __builtin_amdgcn_cvt_pk_fp8_f32(clamp448(a), clamp448(b), w, false); w = __builtin_amdgcn_cvt_pk_fp8_f32(clamp448(c), clamp448(d), w, true); return (unsigned)w; }
; __device__ __forceinline__ float siluf_(float x) { return x * sigmoidf_(x); }
; __device__ __forceinline__ u32x4 pack8(const f32x4 a, const f32x4 b) { u32x4 w; w.x = cvt_pk_bf16(a[0], a[1]); w.y = cvt_pk_bf16(a[2], a[3]); w.z = cvt_pk_bf16(b[0], b[1]); w.w = cvt_pk_bf16(b[2], b[3]); return w; }
;     __device__ __forceinline__ void operator()(const AccT& acc, const Unit& u, int wr, int wc, int fr, int fq) const {
;     ...
;             for (int m = 0; m < 4; ++m) { const int row = row0 + ai * HALF + m * 16; const float rs = rsc[row]; f32x4 z0, z1;
;                 const i32x4v g0 = __builtin_bit_cast(i32x4v, acc[ai][0][m][0]), g1 = __builtin_bit_cast(i32x4v, acc[ai][0][m][1]), u0 = __builtin_bit_cast(i32x4v, acc[ai][1][m][0]), u1 = __builtin_bit_cast(i32x4v, acc[ai][1][m][1]);
; #pragma unroll
;                 for (int j = 0; j < 4; ++j) { z0[j] = siluf_((float)g0[j] * (rs * cg0[j])) * ((float)u0[j] * (rs * cu0[j])); z1[j] = siluf_((float)g1[j] * (rs * cg1[j])) * ((float)u1[j] * (rs * cu1[j])); }
;                 if (sout8 > 0.f) { u32x2 w; w.x = cvt4_fp8(z0[0] * sout8, z0[1] * sout8, z0[2] * sout8, z0[3] * sout8); w.y = cvt4_fp8(z1[0] * sout8, z1[1] * sout8, z1[2] * sout8, z1[3] * sout8); *(u32x2*)((unsigned char*)O + (size_t)row * ldo + cb) = w; }
;                 else *(u32x4*)(O + (size_t)row * ldo + cb) = pack8(z0, z1);
;                 __builtin_amdgcn_sched_barrier(0); }
	v_pk_mul_f32 v[148:149], v[206:207], v[186:187] op_sel_hi:[0,1]
	v_pk_mul_f32 v[150:151], v[206:207], v[188:189] op_sel_hi:[0,1]
	v_pk_add_f32 v[190:191], v[190:191], 1.0 op_sel_hi:[1,0]
	v_pk_add_f32 v[192:193], v[192:193], 1.0 op_sel_hi:[1,0]
	v_pk_add_f32 v[194:195], v[194:195], 1.0 op_sel_hi:[1,0]
	v_pk_add_f32 v[196:197], v[196:197], 1.0 op_sel_hi:[1,0]
	v_rcp_f32_e32 v190, v190
	v_rcp_f32_e32 v191, v191
	v_rcp_f32_e32 v192, v192
	v_rcp_f32_e32 v193, v193
	v_rcp_f32_e32 v194, v194
	v_rcp_f32_e32 v195, v195
	v_rcp_f32_e32 v196, v196
	v_rcp_f32_e32 v197, v197
	v_pk_mul_f32 v[22:23], v[22:23], v[144:145]
	v_pk_mul_f32 v[24:25], v[24:25], v[146:147]
	v_pk_mul_f32 v[18:19], v[18:19], v[148:149]
	v_pk_mul_f32 v[20:21], v[20:21], v[150:151]
	s_mov_b32 s100, 0xdc000
	v_pk_mul_f32 v[22:23], v[22:23], v[190:191]
	v_pk_mul_f32 v[24:25], v[24:25], v[192:193]
	v_pk_mul_f32 v[18:19], v[18:19], v[194:195]
	v_pk_mul_f32 v[20:21], v[20:21], v[196:197]
	v_med3_f32 v22, v22, s58, v181
	v_med3_f32 v23, v23, s58, v181
	v_med3_f32 v24, v24, s58, v181
	v_med3_f32 v25, v25, s58, v181
	v_med3_f32 v18, v18, s58, v181
	v_med3_f32 v19, v19, s58, v181
	v_med3_f32 v20, v20, s58, v181
	v_med3_f32 v21, v21, s58, v181
	v_cvt_pk_fp8_f32 v204, v22, v23
	v_cvt_pk_fp8_f32 v205, v18, v19
	v_lshl_add_u64 v[202:203], v[198:199], 0, s[100:101]
	v_cvt_pk_fp8_f32 v204, v24, v25 op_sel:[0,0,1]
	v_cvt_pk_fp8_f32 v205, v20, v21 op_sel:[0,0,1]
	s_nop 0
	global_store_dwordx2 v[202:203], v[204:205], off nt
	v_cvt_f32_i32_e32 v14, v14
	v_cvt_f32_i32_e32 v15, v15
	v_cvt_f32_i32_e32 v16, v16
	v_cvt_f32_i32_e32 v17, v17
	v_cvt_f32_i32_e32 v10, v10
	v_cvt_f32_i32_e32 v11, v11
	v_cvt_f32_i32_e32 v12, v12
	v_cvt_f32_i32_e32 v13, v13
	v_cvt_f32_i32_e32 v6, v6
	v_cvt_f32_i32_e32 v7, v7
	v_cvt_f32_i32_e32 v8, v8
	v_cvt_f32_i32_e32 v9, v9
	v_cvt_f32_i32_e32 v2, v2
	v_cvt_f32_i32_e32 v3, v3
	v_cvt_f32_i32_e32 v4, v4
	v_cvt_f32_i32_e32 v5, v5
	v_mul_f32_e32 v206, v217, v217
	v_pk_mul_f32 v[136:137], v[216:217], v[132:133] op_sel:[1,0] op_sel_hi:[1,1]
	v_pk_mul_f32 v[138:139], v[216:217], v[134:135] op_sel:[1,0] op_sel_hi:[1,1]
	v_pk_mul_f32 v[140:141], v[216:217], v[154:155] op_sel:[1,0] op_sel_hi:[1,1]
	v_pk_mul_f32 v[142:143], v[216:217], v[156:157] op_sel:[1,0] op_sel_hi:[1,1]
	v_pk_mul_f32 v[190:191], v[14:15], v[136:137]
	v_pk_mul_f32 v[192:193], v[16:17], v[138:139]
	v_pk_mul_f32 v[194:195], v[10:11], v[140:141]
	v_pk_mul_f32 v[196:197], v[12:13], v[142:143]
	v_exp_f32_e32 v190, v190
	v_exp_f32_e32 v191, v191
	v_exp_f32_e32 v192, v192
	v_exp_f32_e32 v193, v193
	v_exp_f32_e32 v194, v194
	v_exp_f32_e32 v195, v195
	v_exp_f32_e32 v196, v196
	v_exp_f32_e32 v197, v197
	v_pk_mul_f32 v[6:7], v[14:15], v[6:7]
	v_pk_mul_f32 v[8:9], v[16:17], v[8:9]
	v_pk_mul_f32 v[2:3], v[10:11], v[2:3]
	v_pk_mul_f32 v[4:5], v[12:13], v[4:5]
	v_pk_mul_f32 v[144:145], v[206:207], v[158:159] op_sel_hi:[0,1]
	v_pk_mul_f32 v[146:147], v[206:207], v[160:161] op_sel_hi:[0,1]
	v_pk_mul_f32 v[148:149], v[206:207], v[186:187] op_sel_hi:[0,1]
	v_pk_mul_f32 v[150:151], v[206:207], v[188:189] op_sel_hi:[0,1]
	v_pk_add_f32 v[190:191], v[190:191], 1.0 op_sel_hi:[1,0]
	v_pk_add_f32 v[192:193], v[192:193], 1.0 op_sel_hi:[1,0]
	v_pk_add_f32 v[194:195], v[194:195], 1.0 op_sel_hi:[1,0]
	v_pk_add_f32 v[196:197], v[196:197], 1.0 op_sel_hi:[1,0]
	v_rcp_f32_e32 v190, v190
	v_rcp_f32_e32 v191, v191
	v_rcp_f32_e32 v192, v192
	v_rcp_f32_e32 v193, v193
	v_rcp_f32_e32 v194, v194
	v_rcp_f32_e32 v195, v195
	v_rcp_f32_e32 v196, v196
	v_rcp_f32_e32 v197, v197
	v_pk_mul_f32 v[6:7], v[6:7], v[144:145]
	v_pk_mul_f32 v[8:9], v[8:9], v[146:147]
	v_pk_mul_f32 v[2:3], v[2:3], v[148:149]
	v_pk_mul_f32 v[4:5], v[4:5], v[150:151]
	s_mov_b32 s100, 0xf2000
	v_pk_mul_f32 v[6:7], v[6:7], v[190:191]
	v_pk_mul_f32 v[8:9], v[8:9], v[192:193]
	v_pk_mul_f32 v[2:3], v[2:3], v[194:195]
	v_pk_mul_f32 v[4:5], v[4:5], v[196:197]
	v_med3_f32 v6, v6, s58, v181
	v_med3_f32 v7, v7, s58, v181
	v_med3_f32 v8, v8, s58, v181
	v_med3_f32 v9, v9, s58, v181
	v_med3_f32 v2, v2, s58, v181
	v_med3_f32 v3, v3, s58, v181
	v_med3_f32 v4, v4, s58, v181
	v_med3_f32 v5, v5, s58, v181
	v_cvt_pk_fp8_f32 v204, v6, v7
	v_cvt_pk_fp8_f32 v205, v2, v3
	v_lshl_add_u64 v[202:203], v[198:199], 0, s[100:101]
	v_cvt_pk_fp8_f32 v204, v8, v9 op_sel:[0,0,1]
	v_cvt_pk_fp8_f32 v205, v4, v5 op_sel:[0,0,1]
	s_nop 0
	global_store_dwordx2 v[202:203], v[204:205], off nt
	s_andn2_b64 vcc, exec, s[28:29]
	s_mov_b64 s[28:29], -1
	s_cbranch_vccnz .LBB0_1408
	s_andn2_b64 vcc, exec, s[4:5]
	s_cbranch_vccnz .LBB0_1407
	s_barrier
	s_branch .LBB0_1407

; __device__ __forceinline__ unsigned cvt4_fp8(float a, float b, float c, float d) { int w = 0; w = __builtin_amdgcn_cvt_pk_fp8_f32(clamp448(a), clamp448(b), w, false); w = __builtin_amdgcn_cvt_pk_fp8_f32(clamp448(c), clamp448(d), w, true); return (unsigned)w; }
; __device__ __forceinline__ float siluf_(float x) { return x * sigmoidf_(x); }
;     __device__ __forceinline__ void operator()(const AccT& acc, const Unit& u, int wr, int wc, int fr, int fq) const {
;         const int rl0 = wr * 64 + fr, cb = u.pn * 128 + wc * 32 + 8 * fq, nb = u.g * 14336 + u.pn * 256 + wc * 32 + 8 * fq;
;         const float* rs_p = rsc + (size_t)u.g * ML + u.pm * BM;
;         f32x4 cg0 = *(const f32x4*)(cmax + nb) * (1.0f / 127.0f), cg1 = *(const f32x4*)(cmax + nb + 4) * (1.0f / 127.0f), cu0 = *(const f32x4*)(cmax + nb + 128) * (1.0f / 127.0f), cu1 = *(const f32x4*)(cmax + nb + 132) * (1.0f / 127.0f);
; #pragma unroll
;         for (int ai = 0; ai < 2; ++ai)
; #pragma unroll
;             for (int m = 0; m < 4; ++m) { const int rl = rl0 + ai * HALF + m * 16; const float rs = rs_p[rl]; f32x4 z0, z1;
;                 const i32x4v g0 = __builtin_bit_cast(i32x4v, acc[ai][0][m][0]), g1 = __builtin_bit_cast(i32x4v, acc[ai][0][m][1]), u0 = __builtin_bit_cast(i32x4v, acc[ai][1][m][0]), u1 = __builtin_bit_cast(i32x4v, acc[ai][1][m][1]);
; #pragma unroll
;                 for (int j = 0; j < 4; ++j) { z0[j] = siluf_((float)g0[j] * (rs * cg0[j])) * ((float)u0[j] * (rs * cu0[j])); z1[j] = siluf_((float)g1[j] * (rs * cg1[j])) * ((float)u1[j] * (rs * cu1[j])); }
;                 u32x2 w; w.x = cvt4_fp8(z0[0] * sout8, z0[1] * sout8, z0[2] * sout8, z0[3] * sout8); w.y = cvt4_fp8(z1[0] * sout8, z1[1] * sout8, z1[2] * sout8, z1[3] * sout8);
;                 *(u32x2*)(O + (size_t)(u.orow0 + rl) * ldo + cb) = w;
;                 __builtin_amdgcn_sched_barrier(0); }
.LBB0_2553:
	v_mul_lo_u32 v130, v168, s70
	s_lshl_b32 s4, s44, 8
	v_add_u32_e32 v130, s4, v130
	v_or_b32_e32 v130, v130, v183
	v_ashrrev_i32_e32 v131, 31, v130
	v_lshl_add_u64 v[130:131], v[130:131], 2, s[24:25]
	v_ashrrev_i32_e32 v169, 31, v168
	s_lshl_b32 s4, s74, 8
	global_load_dwordx4 v[134:137], v[130:131], off offset:512
	global_load_dwordx4 v[138:141], v[130:131], off
	global_load_dwordx4 v[142:145], v[130:131], off offset:528
	global_load_dwordx4 v[146:149], v[130:131], off offset:16
	v_lshlrev_b64 v[130:131], 16, v[168:169]
	s_ashr_i32 s5, s4, 31
	v_lshl_add_u64 v[130:131], s[22:23], 0, v[130:131]
	s_lshl_b64 s[4:5], s[4:5], 2
	v_lshl_add_u64 v[132:133], v[130:131], 0, s[4:5]
	s_nop 0
	v_readfirstlane_b32 s4, v132
	v_readfirstlane_b32 s5, v133
	s_nop 0
	s_nop 0
	s_nop 0
	s_nop 0
	s_nop 0
	global_load_dword v150, v185, s[4:5]
	global_load_dword v219, v185, s[4:5] offset:64
	global_load_dword v220, v185, s[4:5] offset:128
	global_load_dword v221, v185, s[4:5] offset:192
	global_load_dword v222, v185, s[4:5] offset:512
	global_load_dword v223, v185, s[4:5] offset:576
	global_load_dword v224, v185, s[4:5] offset:640
	global_load_dword v225, v185, s[4:5] offset:704
	s_nop 0
	s_nop 0
	s_nop 0
	s_nop 0
	s_nop 0
	s_nop 0
	s_nop 0
	s_nop 0
	v_lshl_or_b32 v130, s44, 7, v183
	v_ashrrev_i32_e32 v131, 31, v130
	s_waitcnt vmcnt(0)
	s_mov_b32 s98, 0xbc3a1e78
	s_mov_b32 s100, 0x39820610
	v_pk_mul_f32 v[132:133], v[138:139], s[98:99] op_sel_hi:[1,0]
	v_pk_mul_f32 v[152:153], v[140:141], s[98:99] op_sel_hi:[1,0]
	v_pk_mul_f32 v[154:155], v[146:147], s[98:99] op_sel_hi:[1,0]
	v_pk_mul_f32 v[156:157], v[148:149], s[98:99] op_sel_hi:[1,0]
	v_pk_mul_f32 v[158:159], v[138:139], v[134:135]
	v_pk_mul_f32 v[160:161], v[140:141], v[136:137]
	v_pk_mul_f32 v[194:195], v[146:147], v[142:143]
	v_pk_mul_f32 v[196:197], v[148:149], v[144:145]
	v_add_u32_e32 v215, v190, v164
	v_mov_b64_e32 v[208:209], s[20:21]
	v_pk_mul_f32 v[158:159], v[158:159], s[100:101] op_sel_hi:[1,0]
	v_pk_mul_f32 v[160:161], v[160:161], s[100:101] op_sel_hi:[1,0]
	v_pk_mul_f32 v[194:195], v[194:195], s[100:101] op_sel_hi:[1,0]
	v_pk_mul_f32 v[196:197], v[196:197], s[100:101] op_sel_hi:[1,0]
	v_mad_i64_i32 v[206:207], s[6:7], v215, s72, v[208:209]
	v_lshl_add_u64 v[206:207], v[206:207], 0, v[130:131]
	s_mov_b32 s5, 0
	v_cvt_f32_i32_e32 v126, v126
	v_cvt_f32_i32_e32 v127, v127
	v_cvt_f32_i32_e32 v128, v128
	v_cvt_f32_i32_e32 v129, v129
	v_cvt_f32_i32_e32 v118, v118
	v_cvt_f32_i32_e32 v119, v119
	v_cvt_f32_i32_e32 v120, v120
	v_cvt_f32_i32_e32 v121, v121
	v_cvt_f32_i32_e32 v122, v122
	v_cvt_f32_i32_e32 v123, v123
	v_cvt_f32_i32_e32 v124, v124
	v_cvt_f32_i32_e32 v125, v125
	v_cvt_f32_i32_e32 v114, v114
	v_cvt_f32_i32_e32 v115, v115
	v_cvt_f32_i32_e32 v116, v116
	v_cvt_f32_i32_e32 v117, v117
	v_mul_f32_e32 v214, v150, v150
	v_pk_mul_f32 v[134:135], v[150:151], v[132:133] op_sel_hi:[0,1]
	v_pk_mul_f32 v[136:137], v[150:151], v[152:153] op_sel_hi:[0,1]
	v_pk_mul_f32 v[138:139], v[150:151], v[154:155] op_sel_hi:[0,1]
	v_pk_mul_f32 v[140:141], v[150:151], v[156:157] op_sel_hi:[0,1]
	v_pk_mul_f32 v[198:199], v[126:127], v[134:135]
	v_pk_mul_f32 v[200:201], v[128:129], v[136:137]
	v_pk_mul_f32 v[202:203], v[118:119], v[138:139]
	v_pk_mul_f32 v[204:205], v[120:121], v[140:141]
	v_exp_f32_e32 v198, v198
	v_exp_f32_e32 v199, v199
	v_exp_f32_e32 v200, v200
	v_exp_f32_e32 v201, v201
	v_exp_f32_e32 v202, v202
	v_exp_f32_e32 v203, v203
	v_exp_f32_e32 v204, v204
	v_exp_f32_e32 v205, v205
	v_pk_mul_f32 v[122:123], v[126:127], v[122:123]
	v_pk_mul_f32 v[124:125], v[128:129], v[124:125]
	v_pk_mul_f32 v[114:115], v[118:119], v[114:115]
	v_pk_mul_f32 v[116:117], v[120:121], v[116:117]
	v_pk_mul_f32 v[142:143], v[214:215], v[158:159] op_sel_hi:[0,1]
	v_pk_mul_f32 v[144:145], v[214:215], v[160:161] op_sel_hi:[0,1]
	v_pk_mul_f32 v[146:147], v[214:215], v[194:195] op_sel_hi:[0,1]
	v_pk_mul_f32 v[148:149], v[214:215], v[196:197] op_sel_hi:[0,1]
	v_pk_add_f32 v[198:199], v[198:199], 1.0 op_sel_hi:[1,0]
	v_pk_add_f32 v[200:201], v[200:201], 1.0 op_sel_hi:[1,0]
	v_pk_add_f32 v[202:203], v[202:203], 1.0 op_sel_hi:[1,0]
	v_pk_add_f32 v[204:205], v[204:205], 1.0 op_sel_hi:[1,0]
	v_rcp_f32_e32 v198, v198
	v_rcp_f32_e32 v199, v199
	v_rcp_f32_e32 v200, v200
	v_rcp_f32_e32 v201, v201
	v_rcp_f32_e32 v202, v202
	v_rcp_f32_e32 v203, v203
	v_rcp_f32_e32 v204, v204
	v_rcp_f32_e32 v205, v205
	v_pk_mul_f32 v[122:123], v[122:123], v[142:143]
	v_pk_mul_f32 v[124:125], v[124:125], v[144:145]
	v_pk_mul_f32 v[114:115], v[114:115], v[146:147]
	v_pk_mul_f32 v[116:117], v[116:117], v[148:149]
	s_mov_b32 s4, 0x0
	v_pk_mul_f32 v[122:123], v[122:123], v[198:199]
	v_pk_mul_f32 v[124:125], v[124:125], v[200:201]
	v_pk_mul_f32 v[114:115], v[114:115], v[202:203]
	v_pk_mul_f32 v[116:117], v[116:117], v[204:205]
	v_med3_f32 v122, v122, s71, v187
	v_med3_f32 v123, v123, s71, v187
	v_med3_f32 v124, v124, s71, v187
	v_med3_f32 v125, v125, s71, v187
	v_med3_f32 v114, v114, s71, v187
	v_med3_f32 v115, v115, s71, v187
	v_med3_f32 v116, v116, s71, v187
	v_med3_f32 v117, v117, s71, v187
	v_cvt_pk_fp8_f32 v212, v122, v123
	v_cvt_pk_fp8_f32 v213, v114, v115
	v_lshl_add_u64 v[210:211], v[206:207], 0, s[4:5]
	v_cvt_pk_fp8_f32 v212, v124, v125 op_sel:[0,0,1]
	v_cvt_pk_fp8_f32 v213, v116, v117 op_sel:[0,0,1]
	s_nop 0
	global_store_dwordx2 v[210:211], v[212:213], off nt
	v_cvt_f32_i32_e32 v110, v110
	v_cvt_f32_i32_e32 v111, v111
	v_cvt_f32_i32_e32 v112, v112
	v_cvt_f32_i32_e32 v113, v113
	v_cvt_f32_i32_e32 v106, v106
	v_cvt_f32_i32_e32 v107, v107
	v_cvt_f32_i32_e32 v108, v108
	v_cvt_f32_i32_e32 v109, v109
	v_cvt_f32_i32_e32 v102, v102
	v_cvt_f32_i32_e32 v103, v103
; __device__ __forceinline__ unsigned cvt4_fp8(float a, float b, float c, float d) { int w = 0; w = __builtin_amdgcn_cvt_pk_fp8_f32(clamp448(a), clamp448(b), w, false); w = __builtin_amdgcn_cvt_pk_fp8_f32(clamp448(c), clamp448(d), w, true); return (unsigned)w; }
; __device__ __forceinline__ float siluf_(float x) { return x * sigmoidf_(x); }
;     __device__ __forceinline__ void operator()(const AccT& acc, const Unit& u, int wr, int wc, int fr, int fq) const {
;     ...
;             for (int m = 0; m < 4; ++m) { const int rl = rl0 + ai * HALF + m * 16; const float rs = rs_p[rl]; f32x4 z0, z1;
;                 const i32x4v g0 = __builtin_bit_cast(i32x4v, acc[ai][0][m][0]), g1 = __builtin_bit_cast(i32x4v, acc[ai][0][m][1]), u0 = __builtin_bit_cast(i32x4v, acc[ai][1][m][0]), u1 = __builtin_bit_cast(i32x4v, acc[ai][1][m][1]);
; #pragma unroll
;                 for (int j = 0; j < 4; ++j) { z0[j] = siluf_((float)g0[j] * (rs * cg0[j])) * ((float)u0[j] * (rs * cu0[j])); z1[j] = siluf_((float)g1[j] * (rs * cg1[j])) * ((float)u1[j] * (rs * cu1[j])); }
;                 u32x2 w; w.x = cvt4_fp8(z0[0] * sout8, z0[1] * sout8, z0[2] * sout8, z0[3] * sout8); w.y = cvt4_fp8(z1[0] * sout8, z1[1] * sout8, z1[2] * sout8, z1[3] * sout8);
;                 *(u32x2*)(O + (size_t)(u.orow0 + rl) * ldo + cb) = w;
;                 __builtin_amdgcn_sched_barrier(0); }
	v_cvt_f32_i32_e32 v104, v104
	v_cvt_f32_i32_e32 v105, v105
	v_cvt_f32_i32_e32 v98, v98
	v_cvt_f32_i32_e32 v99, v99
	v_cvt_f32_i32_e32 v100, v100
	v_cvt_f32_i32_e32 v101, v101
	v_mul_f32_e32 v214, v219, v219
	v_pk_mul_f32 v[134:135], v[218:219], v[132:133] op_sel:[1,0] op_sel_hi:[1,1]
	v_pk_mul_f32 v[136:137], v[218:219], v[152:153] op_sel:[1,0] op_sel_hi:[1,1]
	v_pk_mul_f32 v[138:139], v[218:219], v[154:155] op_sel:[1,0] op_sel_hi:[1,1]
	v_pk_mul_f32 v[140:141], v[218:219], v[156:157] op_sel:[1,0] op_sel_hi:[1,1]
	v_pk_mul_f32 v[198:199], v[110:111], v[134:135]
	v_pk_mul_f32 v[200:201], v[112:113], v[136:137]
	v_pk_mul_f32 v[202:203], v[106:107], v[138:139]
	v_pk_mul_f32 v[204:205], v[108:109], v[140:141]
	v_exp_f32_e32 v198, v198
	v_exp_f32_e32 v199, v199
	v_exp_f32_e32 v200, v200
	v_exp_f32_e32 v201, v201
	v_exp_f32_e32 v202, v202
	v_exp_f32_e32 v203, v203
	v_exp_f32_e32 v204, v204
	v_exp_f32_e32 v205, v205
	v_pk_mul_f32 v[102:103], v[110:111], v[102:103]
	v_pk_mul_f32 v[104:105], v[112:113], v[104:105]
	v_pk_mul_f32 v[98:99], v[106:107], v[98:99]
	v_pk_mul_f32 v[100:101], v[108:109], v[100:101]
	v_pk_mul_f32 v[142:143], v[214:215], v[158:159] op_sel_hi:[0,1]
	v_pk_mul_f32 v[144:145], v[214:215], v[160:161] op_sel_hi:[0,1]
	v_pk_mul_f32 v[146:147], v[214:215], v[194:195] op_sel_hi:[0,1]
	v_pk_mul_f32 v[148:149], v[214:215], v[196:197] op_sel_hi:[0,1]
	v_pk_add_f32 v[198:199], v[198:199], 1.0 op_sel_hi:[1,0]
	v_pk_add_f32 v[200:201], v[200:201], 1.0 op_sel_hi:[1,0]
	v_pk_add_f32 v[202:203], v[202:203], 1.0 op_sel_hi:[1,0]
	v_pk_add_f32 v[204:205], v[204:205], 1.0 op_sel_hi:[1,0]
	v_rcp_f32_e32 v198, v198
	v_rcp_f32_e32 v199, v199
	v_rcp_f32_e32 v200, v200
	v_rcp_f32_e32 v201, v201
	v_rcp_f32_e32 v202, v202
	v_rcp_f32_e32 v203, v203
	v_rcp_f32_e32 v204, v204
	v_rcp_f32_e32 v205, v205
	v_pk_mul_f32 v[102:103], v[102:103], v[142:143]
	v_pk_mul_f32 v[104:105], v[104:105], v[144:145]
	v_pk_mul_f32 v[98:99], v[98:99], v[146:147]
	v_pk_mul_f32 v[100:101], v[100:101], v[148:149]
	s_mov_b32 s4, 0x1c000
	v_pk_mul_f32 v[102:103], v[102:103], v[198:199]
	v_pk_mul_f32 v[104:105], v[104:105], v[200:201]
	v_pk_mul_f32 v[98:99], v[98:99], v[202:203]
	v_pk_mul_f32 v[100:101], v[100:101], v[204:205]
	v_med3_f32 v102, v102, s71, v187
	v_med3_f32 v103, v103, s71, v187
	v_med3_f32 v104, v104, s71, v187
	v_med3_f32 v105, v105, s71, v187
	v_med3_f32 v98, v98, s71, v187
	v_med3_f32 v99, v99, s71, v187
	v_med3_f32 v100, v100, s71, v187
	v_med3_f32 v101, v101, s71, v187
	v_cvt_pk_fp8_f32 v212, v102, v103
	v_cvt_pk_fp8_f32 v213, v98, v99
	v_lshl_add_u64 v[210:211], v[206:207], 0, s[4:5]
	v_cvt_pk_fp8_f32 v212, v104, v105 op_sel:[0,0,1]
	v_cvt_pk_fp8_f32 v213, v100, v101 op_sel:[0,0,1]
	s_nop 0
	global_store_dwordx2 v[210:211], v[212:213], off nt
	v_cvt_f32_i32_e32 v94, v94
	v_cvt_f32_i32_e32 v95, v95
	v_cvt_f32_i32_e32 v96, v96
	v_cvt_f32_i32_e32 v97, v97
	v_cvt_f32_i32_e32 v90, v90
	v_cvt_f32_i32_e32 v91, v91
	v_cvt_f32_i32_e32 v92, v92
	v_cvt_f32_i32_e32 v93, v93
	v_cvt_f32_i32_e32 v86, v86
	v_cvt_f32_i32_e32 v87, v87
	v_cvt_f32_i32_e32 v88, v88
	v_cvt_f32_i32_e32 v89, v89
	v_cvt_f32_i32_e32 v82, v82
	v_cvt_f32_i32_e32 v83, v83
	v_cvt_f32_i32_e32 v84, v84
	v_cvt_f32_i32_e32 v85, v85
	v_mul_f32_e32 v214, v220, v220
	v_pk_mul_f32 v[134:135], v[220:221], v[132:133] op_sel_hi:[0,1]
	v_pk_mul_f32 v[136:137], v[220:221], v[152:153] op_sel_hi:[0,1]
	v_pk_mul_f32 v[138:139], v[220:221], v[154:155] op_sel_hi:[0,1]
	v_pk_mul_f32 v[140:141], v[220:221], v[156:157] op_sel_hi:[0,1]
	v_pk_mul_f32 v[198:199], v[94:95], v[134:135]
	v_pk_mul_f32 v[200:201], v[96:97], v[136:137]
	v_pk_mul_f32 v[202:203], v[90:91], v[138:139]
	v_pk_mul_f32 v[204:205], v[92:93], v[140:141]
	v_exp_f32_e32 v198, v198
	v_exp_f32_e32 v199, v199
	v_exp_f32_e32 v200, v200
	v_exp_f32_e32 v201, v201
	v_exp_f32_e32 v202, v202
	v_exp_f32_e32 v203, v203
	v_exp_f32_e32 v204, v204
	v_exp_f32_e32 v205, v205
	v_pk_mul_f32 v[86:87], v[94:95], v[86:87]
	v_pk_mul_f32 v[88:89], v[96:97], v[88:89]
	v_pk_mul_f32 v[82:83], v[90:91], v[82:83]
	v_pk_mul_f32 v[84:85], v[92:93], v[84:85]
	v_pk_mul_f32 v[142:143], v[214:215], v[158:159] op_sel_hi:[0,1]
	v_pk_mul_f32 v[144:145], v[214:215], v[160:161] op_sel_hi:[0,1]
	v_pk_mul_f32 v[146:147], v[214:215], v[194:195] op_sel_hi:[0,1]
	v_pk_mul_f32 v[148:149], v[214:215], v[196:197] op_sel_hi:[0,1]
	v_pk_add_f32 v[198:199], v[198:199], 1.0 op_sel_hi:[1,0]
	v_pk_add_f32 v[200:201], v[200:201], 1.0 op_sel_hi:[1,0]
	v_pk_add_f32 v[202:203], v[202:203], 1.0 op_sel_hi:[1,0]
	v_pk_add_f32 v[204:205], v[204:205], 1.0 op_sel_hi:[1,0]
	v_rcp_f32_e32 v198, v198
	v_rcp_f32_e32 v199, v199
	v_rcp_f32_e32 v200, v200
	v_rcp_f32_e32 v201, v201
	v_rcp_f32_e32 v202, v202
	v_rcp_f32_e32 v203, v203
	v_rcp_f32_e32 v204, v204
	v_rcp_f32_e32 v205, v205
	v_pk_mul_f32 v[86:87], v[86:87], v[142:143]
	v_pk_mul_f32 v[88:89], v[88:89], v[144:145]
	v_pk_mul_f32 v[82:83], v[82:83], v[146:147]
	v_pk_mul_f32 v[84:85], v[84:85], v[148:149]
	s_mov_b32 s4, 0x38000
	v_pk_mul_f32 v[86:87], v[86:87], v[198:199]
	v_pk_mul_f32 v[88:89], v[88:89], v[200:201]
	v_pk_mul_f32 v[82:83], v[82:83], v[202:203]
	v_pk_mul_f32 v[84:85], v[84:85], v[204:205]
	v_med3_f32 v86, v86, s71, v187
	v_med3_f32 v87, v87, s71, v187
	v_med3_f32 v88, v88, s71, v187
	v_med3_f32 v89, v89, s71, v187
	v_med3_f32 v82, v82, s71, v187
	v_med3_f32 v83, v83, s71, v187
	v_med3_f32 v84, v84, s71, v187
	v_med3_f32 v85, v85, s71, v187
	v_cvt_pk_fp8_f32 v212, v86, v87
	v_cvt_pk_fp8_f32 v213, v82, v83
	v_lshl_add_u64 v[210:211], v[206:207], 0, s[4:5]
	v_cvt_pk_fp8_f32 v212, v88, v89 op_sel:[0,0,1]
	v_cvt_pk_fp8_f32 v213, v84, v85 op_sel:[0,0,1]
	s_nop 0
; __device__ __forceinline__ unsigned cvt4_fp8(float a, float b, float c, float d) { int w = 0; w = __builtin_amdgcn_cvt_pk_fp8_f32(clamp448(a), clamp448(b), w, false); w = __builtin_amdgcn_cvt_pk_fp8_f32(clamp448(c), clamp448(d), w, true); return (unsigned)w; }
; __device__ __forceinline__ float siluf_(float x) { return x * sigmoidf_(x); }
;     __device__ __forceinline__ void operator()(const AccT& acc, const Unit& u, int wr, int wc, int fr, int fq) const {
;     ...
;             for (int m = 0; m < 4; ++m) { const int rl = rl0 + ai * HALF + m * 16; const float rs = rs_p[rl]; f32x4 z0, z1;
;                 const i32x4v g0 = __builtin_bit_cast(i32x4v, acc[ai][0][m][0]), g1 = __builtin_bit_cast(i32x4v, acc[ai][0][m][1]), u0 = __builtin_bit_cast(i32x4v, acc[ai][1][m][0]), u1 = __builtin_bit_cast(i32x4v, acc[ai][1][m][1]);
; #pragma unroll
;                 for (int j = 0; j < 4; ++j) { z0[j] = siluf_((float)g0[j] * (rs * cg0[j])) * ((float)u0[j] * (rs * cu0[j])); z1[j] = siluf_((float)g1[j] * (rs * cg1[j])) * ((float)u1[j] * (rs * cu1[j])); }
;                 u32x2 w; w.x = cvt4_fp8(z0[0] * sout8, z0[1] * sout8, z0[2] * sout8, z0[3] * sout8); w.y = cvt4_fp8(z1[0] * sout8, z1[1] * sout8, z1[2] * sout8, z1[3] * sout8);
;                 *(u32x2*)(O + (size_t)(u.orow0 + rl) * ldo + cb) = w;
;                 __builtin_amdgcn_sched_barrier(0); }
	global_store_dwordx2 v[210:211], v[212:213], off nt
	v_cvt_f32_i32_e32 v78, v78
	v_cvt_f32_i32_e32 v79, v79
	v_cvt_f32_i32_e32 v80, v80
	v_cvt_f32_i32_e32 v81, v81
	v_cvt_f32_i32_e32 v74, v74
	v_cvt_f32_i32_e32 v75, v75
	v_cvt_f32_i32_e32 v76, v76
	v_cvt_f32_i32_e32 v77, v77
	v_cvt_f32_i32_e32 v70, v70
	v_cvt_f32_i32_e32 v71, v71
	v_cvt_f32_i32_e32 v72, v72
	v_cvt_f32_i32_e32 v73, v73
	v_cvt_f32_i32_e32 v66, v66
	v_cvt_f32_i32_e32 v67, v67
	v_cvt_f32_i32_e32 v68, v68
	v_cvt_f32_i32_e32 v69, v69
	v_mul_f32_e32 v214, v221, v221
	v_pk_mul_f32 v[134:135], v[220:221], v[132:133] op_sel:[1,0] op_sel_hi:[1,1]
	v_pk_mul_f32 v[136:137], v[220:221], v[152:153] op_sel:[1,0] op_sel_hi:[1,1]
	v_pk_mul_f32 v[138:139], v[220:221], v[154:155] op_sel:[1,0] op_sel_hi:[1,1]
	v_pk_mul_f32 v[140:141], v[220:221], v[156:157] op_sel:[1,0] op_sel_hi:[1,1]
	v_pk_mul_f32 v[198:199], v[78:79], v[134:135]
	v_pk_mul_f32 v[200:201], v[80:81], v[136:137]
	v_pk_mul_f32 v[202:203], v[74:75], v[138:139]
	v_pk_mul_f32 v[204:205], v[76:77], v[140:141]
	v_exp_f32_e32 v198, v198
	v_exp_f32_e32 v199, v199
	v_exp_f32_e32 v200, v200
	v_exp_f32_e32 v201, v201
	v_exp_f32_e32 v202, v202
	v_exp_f32_e32 v203, v203
	v_exp_f32_e32 v204, v204
	v_exp_f32_e32 v205, v205
	v_pk_mul_f32 v[70:71], v[78:79], v[70:71]
	v_pk_mul_f32 v[72:73], v[80:81], v[72:73]
	v_pk_mul_f32 v[66:67], v[74:75], v[66:67]
	v_pk_mul_f32 v[68:69], v[76:77], v[68:69]
	v_pk_mul_f32 v[142:143], v[214:215], v[158:159] op_sel_hi:[0,1]
	v_pk_mul_f32 v[144:145], v[214:215], v[160:161] op_sel_hi:[0,1]
	v_pk_mul_f32 v[146:147], v[214:215], v[194:195] op_sel_hi:[0,1]
	v_pk_mul_f32 v[148:149], v[214:215], v[196:197] op_sel_hi:[0,1]
	v_pk_add_f32 v[198:199], v[198:199], 1.0 op_sel_hi:[1,0]
	v_pk_add_f32 v[200:201], v[200:201], 1.0 op_sel_hi:[1,0]
	v_pk_add_f32 v[202:203], v[202:203], 1.0 op_sel_hi:[1,0]
	v_pk_add_f32 v[204:205], v[204:205], 1.0 op_sel_hi:[1,0]
	v_rcp_f32_e32 v198, v198
	v_rcp_f32_e32 v199, v199
	v_rcp_f32_e32 v200, v200
	v_rcp_f32_e32 v201, v201
	v_rcp_f32_e32 v202, v202
	v_rcp_f32_e32 v203, v203
	v_rcp_f32_e32 v204, v204
	v_rcp_f32_e32 v205, v205
	v_pk_mul_f32 v[70:71], v[70:71], v[142:143]
	v_pk_mul_f32 v[72:73], v[72:73], v[144:145]
	v_pk_mul_f32 v[66:67], v[66:67], v[146:147]
	v_pk_mul_f32 v[68:69], v[68:69], v[148:149]
	s_mov_b32 s4, 0x54000
	v_pk_mul_f32 v[70:71], v[70:71], v[198:199]
	v_pk_mul_f32 v[72:73], v[72:73], v[200:201]
	v_pk_mul_f32 v[66:67], v[66:67], v[202:203]
	v_pk_mul_f32 v[68:69], v[68:69], v[204:205]
	v_med3_f32 v70, v70, s71, v187
	v_med3_f32 v71, v71, s71, v187
	v_med3_f32 v72, v72, s71, v187
	v_med3_f32 v73, v73, s71, v187
	v_med3_f32 v66, v66, s71, v187
	v_med3_f32 v67, v67, s71, v187
	v_med3_f32 v68, v68, s71, v187
	v_med3_f32 v69, v69, s71, v187
	v_cvt_pk_fp8_f32 v212, v70, v71
	v_cvt_pk_fp8_f32 v213, v66, v67
	v_lshl_add_u64 v[210:211], v[206:207], 0, s[4:5]
	v_cvt_pk_fp8_f32 v212, v72, v73 op_sel:[0,0,1]
	v_cvt_pk_fp8_f32 v213, v68, v69 op_sel:[0,0,1]
	s_nop 0
	global_store_dwordx2 v[210:211], v[212:213], off nt
	v_cvt_f32_i32_e32 v62, v62
	v_cvt_f32_i32_e32 v63, v63
	v_cvt_f32_i32_e32 v64, v64
	v_cvt_f32_i32_e32 v65, v65
	v_cvt_f32_i32_e32 v58, v58
	v_cvt_f32_i32_e32 v59, v59
	v_cvt_f32_i32_e32 v60, v60
	v_cvt_f32_i32_e32 v61, v61
	v_cvt_f32_i32_e32 v54, v54
	v_cvt_f32_i32_e32 v55, v55
	v_cvt_f32_i32_e32 v56, v56
	v_cvt_f32_i32_e32 v57, v57
	v_cvt_f32_i32_e32 v50, v50
	v_cvt_f32_i32_e32 v51, v51
	v_cvt_f32_i32_e32 v52, v52
	v_cvt_f32_i32_e32 v53, v53
	v_mul_f32_e32 v214, v222, v222
	v_pk_mul_f32 v[134:135], v[222:223], v[132:133] op_sel_hi:[0,1]
	v_pk_mul_f32 v[136:137], v[222:223], v[152:153] op_sel_hi:[0,1]
	v_pk_mul_f32 v[138:139], v[222:223], v[154:155] op_sel_hi:[0,1]
	v_pk_mul_f32 v[140:141], v[222:223], v[156:157] op_sel_hi:[0,1]
	v_pk_mul_f32 v[198:199], v[62:63], v[134:135]
	v_pk_mul_f32 v[200:201], v[64:65], v[136:137]
	v_pk_mul_f32 v[202:203], v[58:59], v[138:139]
	v_pk_mul_f32 v[204:205], v[60:61], v[140:141]
	v_exp_f32_e32 v198, v198
	v_exp_f32_e32 v199, v199
	v_exp_f32_e32 v200, v200
	v_exp_f32_e32 v201, v201
	v_exp_f32_e32 v202, v202
	v_exp_f32_e32 v203, v203
	v_exp_f32_e32 v204, v204
	v_exp_f32_e32 v205, v205
	v_pk_mul_f32 v[54:55], v[62:63], v[54:55]
	v_pk_mul_f32 v[56:57], v[64:65], v[56:57]
	v_pk_mul_f32 v[50:51], v[58:59], v[50:51]
	v_pk_mul_f32 v[52:53], v[60:61], v[52:53]
	v_pk_mul_f32 v[142:143], v[214:215], v[158:159] op_sel_hi:[0,1]
	v_pk_mul_f32 v[144:145], v[214:215], v[160:161] op_sel_hi:[0,1]
	v_pk_mul_f32 v[146:147], v[214:215], v[194:195] op_sel_hi:[0,1]
	v_pk_mul_f32 v[148:149], v[214:215], v[196:197] op_sel_hi:[0,1]
	v_pk_add_f32 v[198:199], v[198:199], 1.0 op_sel_hi:[1,0]
	v_pk_add_f32 v[200:201], v[200:201], 1.0 op_sel_hi:[1,0]
	v_pk_add_f32 v[202:203], v[202:203], 1.0 op_sel_hi:[1,0]
	v_pk_add_f32 v[204:205], v[204:205], 1.0 op_sel_hi:[1,0]
	v_rcp_f32_e32 v198, v198
	v_rcp_f32_e32 v199, v199
	v_rcp_f32_e32 v200, v200
	v_rcp_f32_e32 v201, v201
	v_rcp_f32_e32 v202, v202
	v_rcp_f32_e32 v203, v203
	v_rcp_f32_e32 v204, v204
	v_rcp_f32_e32 v205, v205
	v_pk_mul_f32 v[54:55], v[54:55], v[142:143]
	v_pk_mul_f32 v[56:57], v[56:57], v[144:145]
	v_pk_mul_f32 v[50:51], v[50:51], v[146:147]
	v_pk_mul_f32 v[52:53], v[52:53], v[148:149]
	s_mov_b32 s4, 0xe0000
	v_pk_mul_f32 v[54:55], v[54:55], v[198:199]
	v_pk_mul_f32 v[56:57], v[56:57], v[200:201]
	v_pk_mul_f32 v[50:51], v[50:51], v[202:203]
	v_pk_mul_f32 v[52:53], v[52:53], v[204:205]
	v_med3_f32 v54, v54, s71, v187
	v_med3_f32 v55, v55, s71, v187
	v_med3_f32 v56, v56, s71, v187
	v_med3_f32 v57, v57, s71, v187
	v_med3_f32 v50, v50, s71, v187
	v_med3_f32 v51, v51, s71, v187
	v_med3_f32 v52, v52, s71, v187
; __device__ __forceinline__ unsigned cvt4_fp8(float a, float b, float c, float d) { int w = 0; w = __builtin_amdgcn_cvt_pk_fp8_f32(clamp448(a), clamp448(b), w, false); w = __builtin_amdgcn_cvt_pk_fp8_f32(clamp448(c), clamp448(d), w, true); return (unsigned)w; }
; __device__ __forceinline__ float siluf_(float x) { return x * sigmoidf_(x); }
;     __device__ __forceinline__ void operator()(const AccT& acc, const Unit& u, int wr, int wc, int fr, int fq) const {
;     ...
;             for (int m = 0; m < 4; ++m) { const int rl = rl0 + ai * HALF + m * 16; const float rs = rs_p[rl]; f32x4 z0, z1;
;                 const i32x4v g0 = __builtin_bit_cast(i32x4v, acc[ai][0][m][0]), g1 = __builtin_bit_cast(i32x4v, acc[ai][0][m][1]), u0 = __builtin_bit_cast(i32x4v, acc[ai][1][m][0]), u1 = __builtin_bit_cast(i32x4v, acc[ai][1][m][1]);
; #pragma unroll
;                 for (int j = 0; j < 4; ++j) { z0[j] = siluf_((float)g0[j] * (rs * cg0[j])) * ((float)u0[j] * (rs * cu0[j])); z1[j] = siluf_((float)g1[j] * (rs * cg1[j])) * ((float)u1[j] * (rs * cu1[j])); }
;                 u32x2 w; w.x = cvt4_fp8(z0[0] * sout8, z0[1] * sout8, z0[2] * sout8, z0[3] * sout8); w.y = cvt4_fp8(z1[0] * sout8, z1[1] * sout8, z1[2] * sout8, z1[3] * sout8);
;                 *(u32x2*)(O + (size_t)(u.orow0 + rl) * ldo + cb) = w;
;                 __builtin_amdgcn_sched_barrier(0); }
	v_med3_f32 v53, v53, s71, v187
	v_cvt_pk_fp8_f32 v212, v54, v55
	v_cvt_pk_fp8_f32 v213, v50, v51
	v_lshl_add_u64 v[210:211], v[206:207], 0, s[4:5]
	v_cvt_pk_fp8_f32 v212, v56, v57 op_sel:[0,0,1]
	v_cvt_pk_fp8_f32 v213, v52, v53 op_sel:[0,0,1]
	s_nop 0
	global_store_dwordx2 v[210:211], v[212:213], off nt
	v_cvt_f32_i32_e32 v46, v46
	v_cvt_f32_i32_e32 v47, v47
	v_cvt_f32_i32_e32 v48, v48
	v_cvt_f32_i32_e32 v49, v49
	v_cvt_f32_i32_e32 v42, v42
	v_cvt_f32_i32_e32 v43, v43
	v_cvt_f32_i32_e32 v44, v44
	v_cvt_f32_i32_e32 v45, v45
	v_cvt_f32_i32_e32 v38, v38
	v_cvt_f32_i32_e32 v39, v39
	v_cvt_f32_i32_e32 v40, v40
	v_cvt_f32_i32_e32 v41, v41
	v_cvt_f32_i32_e32 v34, v34
	v_cvt_f32_i32_e32 v35, v35
	v_cvt_f32_i32_e32 v36, v36
	v_cvt_f32_i32_e32 v37, v37
	v_mul_f32_e32 v214, v223, v223
	v_pk_mul_f32 v[134:135], v[222:223], v[132:133] op_sel:[1,0] op_sel_hi:[1,1]
	v_pk_mul_f32 v[136:137], v[222:223], v[152:153] op_sel:[1,0] op_sel_hi:[1,1]
	v_pk_mul_f32 v[138:139], v[222:223], v[154:155] op_sel:[1,0] op_sel_hi:[1,1]
	v_pk_mul_f32 v[140:141], v[222:223], v[156:157] op_sel:[1,0] op_sel_hi:[1,1]
	v_pk_mul_f32 v[198:199], v[46:47], v[134:135]
	v_pk_mul_f32 v[200:201], v[48:49], v[136:137]
	v_pk_mul_f32 v[202:203], v[42:43], v[138:139]
	v_pk_mul_f32 v[204:205], v[44:45], v[140:141]
	v_exp_f32_e32 v198, v198
	v_exp_f32_e32 v199, v199
	v_exp_f32_e32 v200, v200
	v_exp_f32_e32 v201, v201
	v_exp_f32_e32 v202, v202
	v_exp_f32_e32 v203, v203
	v_exp_f32_e32 v204, v204
	v_exp_f32_e32 v205, v205
	v_pk_mul_f32 v[38:39], v[46:47], v[38:39]
	v_pk_mul_f32 v[40:41], v[48:49], v[40:41]
	v_pk_mul_f32 v[34:35], v[42:43], v[34:35]
	v_pk_mul_f32 v[36:37], v[44:45], v[36:37]
	v_pk_mul_f32 v[142:143], v[214:215], v[158:159] op_sel_hi:[0,1]
	v_pk_mul_f32 v[144:145], v[214:215], v[160:161] op_sel_hi:[0,1]
	v_pk_mul_f32 v[146:147], v[214:215], v[194:195] op_sel_hi:[0,1]
	v_pk_mul_f32 v[148:149], v[214:215], v[196:197] op_sel_hi:[0,1]
	v_pk_add_f32 v[198:199], v[198:199], 1.0 op_sel_hi:[1,0]
	v_pk_add_f32 v[200:201], v[200:201], 1.0 op_sel_hi:[1,0]
	v_pk_add_f32 v[202:203], v[202:203], 1.0 op_sel_hi:[1,0]
	v_pk_add_f32 v[204:205], v[204:205], 1.0 op_sel_hi:[1,0]
	v_rcp_f32_e32 v198, v198
	v_rcp_f32_e32 v199, v199
	v_rcp_f32_e32 v200, v200
	v_rcp_f32_e32 v201, v201
	v_rcp_f32_e32 v202, v202
	v_rcp_f32_e32 v203, v203
	v_rcp_f32_e32 v204, v204
	v_rcp_f32_e32 v205, v205
	v_pk_mul_f32 v[38:39], v[38:39], v[142:143]
	v_pk_mul_f32 v[40:41], v[40:41], v[144:145]
	v_pk_mul_f32 v[34:35], v[34:35], v[146:147]
	v_pk_mul_f32 v[36:37], v[36:37], v[148:149]
	s_mov_b32 s4, 0xfc000
	v_pk_mul_f32 v[38:39], v[38:39], v[198:199]
	v_pk_mul_f32 v[40:41], v[40:41], v[200:201]
	v_pk_mul_f32 v[34:35], v[34:35], v[202:203]
	v_pk_mul_f32 v[36:37], v[36:37], v[204:205]
	v_med3_f32 v38, v38, s71, v187
	v_med3_f32 v39, v39, s71, v187
	v_med3_f32 v40, v40, s71, v187
	v_med3_f32 v41, v41, s71, v187
	v_med3_f32 v34, v34, s71, v187
	v_med3_f32 v35, v35, s71, v187
	v_med3_f32 v36, v36, s71, v187
	v_med3_f32 v37, v37, s71, v187
	v_cvt_pk_fp8_f32 v212, v38, v39
	v_cvt_pk_fp8_f32 v213, v34, v35
	v_lshl_add_u64 v[210:211], v[206:207], 0, s[4:5]
	v_cvt_pk_fp8_f32 v212, v40, v41 op_sel:[0,0,1]
	v_cvt_pk_fp8_f32 v213, v36, v37 op_sel:[0,0,1]
	s_nop 0
	global_store_dwordx2 v[210:211], v[212:213], off nt
	v_cvt_f32_i32_e32 v30, v30
	v_cvt_f32_i32_e32 v31, v31
	v_cvt_f32_i32_e32 v32, v32
	v_cvt_f32_i32_e32 v33, v33
	v_cvt_f32_i32_e32 v26, v26
	v_cvt_f32_i32_e32 v27, v27
	v_cvt_f32_i32_e32 v28, v28
	v_cvt_f32_i32_e32 v29, v29
	v_cvt_f32_i32_e32 v22, v22
	v_cvt_f32_i32_e32 v23, v23
	v_cvt_f32_i32_e32 v24, v24
	v_cvt_f32_i32_e32 v25, v25
	v_cvt_f32_i32_e32 v18, v18
	v_cvt_f32_i32_e32 v19, v19
	v_cvt_f32_i32_e32 v20, v20
	v_cvt_f32_i32_e32 v21, v21
	v_mul_f32_e32 v214, v224, v224
	v_pk_mul_f32 v[134:135], v[224:225], v[132:133] op_sel_hi:[0,1]
	v_pk_mul_f32 v[136:137], v[224:225], v[152:153] op_sel_hi:[0,1]
	v_pk_mul_f32 v[138:139], v[224:225], v[154:155] op_sel_hi:[0,1]
	v_pk_mul_f32 v[140:141], v[224:225], v[156:157] op_sel_hi:[0,1]
	v_pk_mul_f32 v[198:199], v[30:31], v[134:135]
	v_pk_mul_f32 v[200:201], v[32:33], v[136:137]
	v_pk_mul_f32 v[202:203], v[26:27], v[138:139]
	v_pk_mul_f32 v[204:205], v[28:29], v[140:141]
	v_exp_f32_e32 v198, v198
	v_exp_f32_e32 v199, v199
	v_exp_f32_e32 v200, v200
	v_exp_f32_e32 v201, v201
	v_exp_f32_e32 v202, v202
	v_exp_f32_e32 v203, v203
	v_exp_f32_e32 v204, v204
	v_exp_f32_e32 v205, v205
	v_pk_mul_f32 v[22:23], v[30:31], v[22:23]
	v_pk_mul_f32 v[24:25], v[32:33], v[24:25]
	v_pk_mul_f32 v[18:19], v[26:27], v[18:19]
	v_pk_mul_f32 v[20:21], v[28:29], v[20:21]
	v_pk_mul_f32 v[142:143], v[214:215], v[158:159] op_sel_hi:[0,1]
; __device__ __forceinline__ unsigned cvt4_fp8(float a, float b, float c, float d) { int w = 0; w = __builtin_amdgcn_cvt_pk_fp8_f32(clamp448(a), clamp448(b), w, false); w = __builtin_amdgcn_cvt_pk_fp8_f32(clamp448(c), clamp448(d), w, true); return (unsigned)w; }
; __device__ __forceinline__ float siluf_(float x) { return x * sigmoidf_(x); }
;     __device__ __forceinline__ void operator()(const AccT& acc, const Unit& u, int wr, int wc, int fr, int fq) const {
;     ...
;             for (int m = 0; m < 4; ++m) { const int rl = rl0 + ai * HALF + m * 16; const float rs = rs_p[rl]; f32x4 z0, z1;
;                 const i32x4v g0 = __builtin_bit_cast(i32x4v, acc[ai][0][m][0]), g1 = __builtin_bit_cast(i32x4v, acc[ai][0][m][1]), u0 = __builtin_bit_cast(i32x4v, acc[ai][1][m][0]), u1 = __builtin_bit_cast(i32x4v, acc[ai][1][m][1]);
; #pragma unroll
;                 for (int j = 0; j < 4; ++j) { z0[j] = siluf_((float)g0[j] * (rs * cg0[j])) * ((float)u0[j] * (rs * cu0[j])); z1[j] = siluf_((float)g1[j] * (rs * cg1[j])) * ((float)u1[j] * (rs * cu1[j])); }
;                 u32x2 w; w.x = cvt4_fp8(z0[0] * sout8, z0[1] * sout8, z0[2] * sout8, z0[3] * sout8); w.y = cvt4_fp8(z1[0] * sout8, z1[1] * sout8, z1[2] * sout8, z1[3] * sout8);
;                 *(u32x2*)(O + (size_t)(u.orow0 + rl) * ldo + cb) = w;
;                 __builtin_amdgcn_sched_barrier(0); }
	v_pk_mul_f32 v[144:145], v[214:215], v[160:161] op_sel_hi:[0,1]
	v_pk_mul_f32 v[146:147], v[214:215], v[194:195] op_sel_hi:[0,1]
	v_pk_mul_f32 v[148:149], v[214:215], v[196:197] op_sel_hi:[0,1]
	v_pk_add_f32 v[198:199], v[198:199], 1.0 op_sel_hi:[1,0]
	v_pk_add_f32 v[200:201], v[200:201], 1.0 op_sel_hi:[1,0]
	v_pk_add_f32 v[202:203], v[202:203], 1.0 op_sel_hi:[1,0]
	v_pk_add_f32 v[204:205], v[204:205], 1.0 op_sel_hi:[1,0]
	v_rcp_f32_e32 v198, v198
	v_rcp_f32_e32 v199, v199
	v_rcp_f32_e32 v200, v200
	v_rcp_f32_e32 v201, v201
	v_rcp_f32_e32 v202, v202
	v_rcp_f32_e32 v203, v203
	v_rcp_f32_e32 v204, v204
	v_rcp_f32_e32 v205, v205
	v_pk_mul_f32 v[22:23], v[22:23], v[142:143]
	v_pk_mul_f32 v[24:25], v[24:25], v[144:145]
	v_pk_mul_f32 v[18:19], v[18:19], v[146:147]
	v_pk_mul_f32 v[20:21], v[20:21], v[148:149]
	s_mov_b32 s4, 0x118000
	v_pk_mul_f32 v[22:23], v[22:23], v[198:199]
	v_pk_mul_f32 v[24:25], v[24:25], v[200:201]
	v_pk_mul_f32 v[18:19], v[18:19], v[202:203]
	v_pk_mul_f32 v[20:21], v[20:21], v[204:205]
	v_med3_f32 v22, v22, s71, v187
	v_med3_f32 v23, v23, s71, v187
	v_med3_f32 v24, v24, s71, v187
	v_med3_f32 v25, v25, s71, v187
	v_med3_f32 v18, v18, s71, v187
	v_med3_f32 v19, v19, s71, v187
	v_med3_f32 v20, v20, s71, v187
	v_med3_f32 v21, v21, s71, v187
	v_cvt_pk_fp8_f32 v212, v22, v23
	v_cvt_pk_fp8_f32 v213, v18, v19
	v_lshl_add_u64 v[210:211], v[206:207], 0, s[4:5]
	v_cvt_pk_fp8_f32 v212, v24, v25 op_sel:[0,0,1]
	v_cvt_pk_fp8_f32 v213, v20, v21 op_sel:[0,0,1]
	s_nop 0
	global_store_dwordx2 v[210:211], v[212:213], off nt
	v_cvt_f32_i32_e32 v14, v14
	v_cvt_f32_i32_e32 v15, v15
	v_cvt_f32_i32_e32 v16, v16
	v_cvt_f32_i32_e32 v17, v17
	v_cvt_f32_i32_e32 v10, v10
	v_cvt_f32_i32_e32 v11, v11
	v_cvt_f32_i32_e32 v12, v12
	v_cvt_f32_i32_e32 v13, v13
	v_cvt_f32_i32_e32 v6, v6
	v_cvt_f32_i32_e32 v7, v7
	v_cvt_f32_i32_e32 v8, v8
	v_cvt_f32_i32_e32 v9, v9
	v_cvt_f32_i32_e32 v2, v2
	v_cvt_f32_i32_e32 v3, v3
	v_cvt_f32_i32_e32 v4, v4
	v_cvt_f32_i32_e32 v5, v5
	v_mul_f32_e32 v214, v225, v225
	v_pk_mul_f32 v[134:135], v[224:225], v[132:133] op_sel:[1,0] op_sel_hi:[1,1]
	v_pk_mul_f32 v[136:137], v[224:225], v[152:153] op_sel:[1,0] op_sel_hi:[1,1]
	v_pk_mul_f32 v[138:139], v[224:225], v[154:155] op_sel:[1,0] op_sel_hi:[1,1]
	v_pk_mul_f32 v[140:141], v[224:225], v[156:157] op_sel:[1,0] op_sel_hi:[1,1]
	v_pk_mul_f32 v[198:199], v[14:15], v[134:135]
	v_pk_mul_f32 v[200:201], v[16:17], v[136:137]
	v_pk_mul_f32 v[202:203], v[10:11], v[138:139]
	v_pk_mul_f32 v[204:205], v[12:13], v[140:141]
	v_exp_f32_e32 v198, v198
	v_exp_f32_e32 v199, v199
	v_exp_f32_e32 v200, v200
	v_exp_f32_e32 v201, v201
	v_exp_f32_e32 v202, v202
	v_exp_f32_e32 v203, v203
	v_exp_f32_e32 v204, v204
	v_exp_f32_e32 v205, v205
	v_pk_mul_f32 v[6:7], v[14:15], v[6:7]
	v_pk_mul_f32 v[8:9], v[16:17], v[8:9]
	v_pk_mul_f32 v[2:3], v[10:11], v[2:3]
	v_pk_mul_f32 v[4:5], v[12:13], v[4:5]
	v_pk_mul_f32 v[142:143], v[214:215], v[158:159] op_sel_hi:[0,1]
	v_pk_mul_f32 v[144:145], v[214:215], v[160:161] op_sel_hi:[0,1]
	v_pk_mul_f32 v[146:147], v[214:215], v[194:195] op_sel_hi:[0,1]
	v_pk_mul_f32 v[148:149], v[214:215], v[196:197] op_sel_hi:[0,1]
	v_pk_add_f32 v[198:199], v[198:199], 1.0 op_sel_hi:[1,0]
	v_pk_add_f32 v[200:201], v[200:201], 1.0 op_sel_hi:[1,0]
	v_pk_add_f32 v[202:203], v[202:203], 1.0 op_sel_hi:[1,0]
	v_pk_add_f32 v[204:205], v[204:205], 1.0 op_sel_hi:[1,0]
	v_rcp_f32_e32 v198, v198
	v_rcp_f32_e32 v199, v199
	v_rcp_f32_e32 v200, v200
	v_rcp_f32_e32 v201, v201
	v_rcp_f32_e32 v202, v202
	v_rcp_f32_e32 v203, v203
	v_rcp_f32_e32 v204, v204
	v_rcp_f32_e32 v205, v205
	v_pk_mul_f32 v[6:7], v[6:7], v[142:143]
	v_pk_mul_f32 v[8:9], v[8:9], v[144:145]
	v_pk_mul_f32 v[2:3], v[2:3], v[146:147]
	v_pk_mul_f32 v[4:5], v[4:5], v[148:149]
	s_mov_b32 s4, 0x134000
	v_pk_mul_f32 v[6:7], v[6:7], v[198:199]
	v_pk_mul_f32 v[8:9], v[8:9], v[200:201]
	v_pk_mul_f32 v[2:3], v[2:3], v[202:203]
	v_pk_mul_f32 v[4:5], v[4:5], v[204:205]
	v_med3_f32 v6, v6, s71, v187
	v_med3_f32 v7, v7, s71, v187
	v_med3_f32 v8, v8, s71, v187
	v_med3_f32 v9, v9, s71, v187
	v_med3_f32 v2, v2, s71, v187
	v_med3_f32 v3, v3, s71, v187
	v_med3_f32 v4, v4, s71, v187
	v_med3_f32 v5, v5, s71, v187
	v_cvt_pk_fp8_f32 v212, v6, v7
	v_cvt_pk_fp8_f32 v213, v2, v3
	v_lshl_add_u64 v[210:211], v[206:207], 0, s[4:5]
	v_cvt_pk_fp8_f32 v212, v8, v9 op_sel:[0,0,1]
	v_cvt_pk_fp8_f32 v213, v4, v5 op_sel:[0,0,1]
	s_nop 0
	global_store_dwordx2 v[210:211], v[212:213], off nt
	s_and_b64 vcc, exec, s[2:3]
	s_mov_b64 s[2:3], -1
	s_cbranch_vccnz .LBB0_2537
	s_andn2_b64 vcc, exec, s[18:19]
	s_cbranch_vccnz .LBB0_2536
	s_barrier
	s_branch .LBB0_2536
